# cache-policy strategy: the once-read gathered fp8 expert-output rows (row pass A layer 1, final pass) are loaded non-temporally
# speedup vs baseline: 1.0051x; 1.0051x over previous
.LBB0_382:
	v_readlane_b32 s10, v254, 8
	s_mov_b32 s12, 0xb00000
	s_mov_b32 s13, 0xa00000
	v_add_u32_e32 v62, s10, v68
	v_add_u32_e32 v64, s10, v87
	s_mov_b32 s10, 35
	s_ashr_i32 s11, s10, 31
	s_lshl_b64 s[10:11], s[10:11], 3
	s_add_u32 s10, s0, s10
	v_lshlrev_b32_e32 v63, 1, v62
	v_max_i32_e32 v62, v64, v62
	s_addc_u32 s11, s1, s11
	v_cmp_gt_i32_e32 vcc, s77, v62
	s_load_dwordx2 s[10:11], s[10:11], 0x0
	s_waitcnt vmcnt(3)
	v_ashrrev_i32_e32 v95, 31, v18
	v_cndmask_b32_e32 v62, v90, v63, vcc
	v_lshlrev_b32_e32 v74, 2, v62
	v_ashrrev_i32_e32 v75, 31, v74
	v_lshlrev_b64 v[62:63], 2, v[74:75]
	s_waitcnt lgkmcnt(0)
	v_lshl_add_u64 v[64:65], s[10:11], 0, v[62:63]
	s_mov_b32 s10, 35
	s_ashr_i32 s11, s10, 31
	s_lshl_b64 s[10:11], s[10:11], 3
	s_add_u32 s10, s0, s10
	s_addc_u32 s11, s1, s11
	s_load_dwordx2 s[10:11], s[10:11], 0x0
	v_or_b32_e32 v74, 4, v74
	v_ashrrev_i32_e32 v75, 31, v74
	v_lshlrev_b64 v[74:75], 2, v[74:75]
	v_mov_b32_e32 v94, v18
	s_waitcnt lgkmcnt(0)
	v_lshl_add_u64 v[66:67], s[10:11], 0, v[62:63]
	v_add_co_u32_e32 v62, vcc, s12, v64
	s_mov_b32 s10, 35
	s_nop 0
	v_addc_co_u32_e32 v63, vcc, 0, v65, vcc
	v_add_co_u32_e32 v66, vcc, s13, v66
	global_load_dwordx4 v[62:65], v[62:63], off
	s_nop 0
	v_addc_co_u32_e32 v67, vcc, 0, v67, vcc
	global_load_dwordx4 v[66:69], v[66:67], off
	s_ashr_i32 s11, s10, 31
	s_lshl_b64 s[10:11], s[10:11], 3
	s_add_u32 s10, s0, s10
	s_addc_u32 s11, s1, s11
	s_load_dwordx2 s[10:11], s[10:11], 0x0
	v_lshlrev_b64 v[94:95], 10, v[94:95]
	v_mov_b32_e32 v85, v1
	s_mov_b64 s[14:15], 0x48800000
	v_lshl_add_u32 v140, v100, 12, v89
	s_waitcnt lgkmcnt(0)
	v_lshl_add_u64 v[76:77], s[10:11], 0, v[74:75]
	s_mov_b32 s10, 35
	s_ashr_i32 s11, s10, 31
	s_lshl_b64 s[10:11], s[10:11], 3
	s_add_u32 s10, s0, s10
	s_addc_u32 s11, s1, s11
	s_load_dwordx2 s[10:11], s[10:11], 0x0
	s_waitcnt lgkmcnt(0)
	v_lshl_add_u64 v[78:79], s[10:11], 0, v[74:75]
	v_add_co_u32_e32 v74, vcc, s12, v76
	s_mov_b32 s10, 35
	s_nop 0
	v_addc_co_u32_e32 v75, vcc, 0, v77, vcc
	v_add_co_u32_e32 v78, vcc, s13, v78
	global_load_dwordx4 v[74:77], v[74:75], off
	s_nop 0
	v_addc_co_u32_e32 v79, vcc, 0, v79, vcc
	global_load_dwordx4 v[78:81], v[78:79], off
	s_ashr_i32 s11, s10, 31
	s_lshl_b64 s[10:11], s[10:11], 3
	s_add_u32 s10, s0, s10
	s_addc_u32 s11, s1, s11
	s_load_dwordx2 s[10:11], s[10:11], 0x0
	s_mov_b32 s12, 0x48800000
	s_waitcnt lgkmcnt(0)
	v_lshl_add_u64 v[94:95], s[10:11], 0, v[94:95]
	v_lshl_add_u64 v[94:95], v[94:95], 0, v[84:85]
	v_lshl_add_u64 v[96:97], v[94:95], 0, s[14:15]
	v_add_co_u32_e32 v94, vcc, s12, v94
	s_mov_b32 s10, 35
	s_nop 0
	v_addc_co_u32_e32 v95, vcc, 0, v95, vcc
	global_load_dword v118, v[94:95], off nt
	global_load_dword v130, v[96:97], off offset:256 nt
	global_load_dword v131, v[96:97], off offset:512 nt
	global_load_dword v112, v[96:97], off offset:768 nt
	s_ashr_i32 s11, s10, 31
	s_lshl_b64 s[10:11], s[10:11], 3
	s_add_u32 s10, s0, s10
	s_addc_u32 s11, s1, s11
	s_load_dwordx2 s[10:11], s[10:11], 0x0
	v_ashrrev_i32_e32 v95, 31, v19
	v_mov_b32_e32 v94, v19
	v_lshlrev_b64 v[94:95], 10, v[94:95]
	s_waitcnt lgkmcnt(0)
	v_lshl_add_u64 v[94:95], s[10:11], 0, v[94:95]
	v_lshl_add_u64 v[94:95], v[94:95], 0, v[84:85]
	v_lshl_add_u64 v[96:97], v[94:95], 0, s[14:15]
	v_add_co_u32_e32 v94, vcc, s12, v94
	s_mov_b32 s10, 35
	s_nop 0
	v_addc_co_u32_e32 v95, vcc, 0, v95, vcc
	global_load_dword v121, v[94:95], off nt
	global_load_dword v132, v[96:97], off offset:256 nt
	global_load_dword v133, v[96:97], off offset:512 nt
	global_load_dword v113, v[96:97], off offset:768 nt
	s_ashr_i32 s11, s10, 31
	s_lshl_b64 s[10:11], s[10:11], 3
	s_add_u32 s10, s0, s10
	s_addc_u32 s11, s1, s11
	s_load_dwordx2 s[10:11], s[10:11], 0x0
	v_ashrrev_i32_e32 v95, 31, v20
	v_mov_b32_e32 v94, v20
	v_lshlrev_b64 v[94:95], 10, v[94:95]
	s_waitcnt lgkmcnt(0)
	v_lshl_add_u64 v[94:95], s[10:11], 0, v[94:95]
	v_lshl_add_u64 v[94:95], v[94:95], 0, v[84:85]
	v_lshl_add_u64 v[96:97], v[94:95], 0, s[14:15]
	v_add_co_u32_e32 v94, vcc, s12, v94
	s_mov_b32 s10, 35
	s_nop 0
	v_addc_co_u32_e32 v95, vcc, 0, v95, vcc
	global_load_dword v125, v[94:95], off nt
	global_load_dword v134, v[96:97], off offset:256 nt
	global_load_dword v135, v[96:97], off offset:512 nt
	global_load_dword v136, v[96:97], off offset:768 nt
	s_ashr_i32 s11, s10, 31
	s_lshl_b64 s[10:11], s[10:11], 3
	s_add_u32 s10, s0, s10
	s_addc_u32 s11, s1, s11
	s_load_dwordx2 s[10:11], s[10:11], 0x0
	v_ashrrev_i32_e32 v95, 31, v21
	v_mov_b32_e32 v94, v21
	v_lshlrev_b64 v[94:95], 10, v[94:95]
	s_waitcnt lgkmcnt(0)
	v_lshl_add_u64 v[94:95], s[10:11], 0, v[94:95]
	v_lshl_add_u64 v[94:95], v[94:95], 0, v[84:85]
	v_lshl_add_u64 v[96:97], v[94:95], 0, s[14:15]
	v_add_co_u32_e32 v94, vcc, s12, v94
	s_mov_b32 s10, 35
	s_nop 0
	v_addc_co_u32_e32 v95, vcc, 0, v95, vcc
	global_load_dword v129, v[94:95], off nt
	global_load_dword v137, v[96:97], off offset:256 nt
	global_load_dword v138, v[96:97], off offset:512 nt
	global_load_dword v139, v[96:97], off offset:768 nt
	s_ashr_i32 s11, s10, 31
	s_lshl_b64 s[10:11], s[10:11], 3
	s_add_u32 s10, s0, s10
	s_addc_u32 s11, s1, s11
	s_load_dwordx2 s[10:11], s[10:11], 0x0
	s_waitcnt vmcnt(21)
	v_ashrrev_i32_e32 v95, 31, v26
	v_mov_b32_e32 v94, v26
	v_lshlrev_b64 v[94:95], 10, v[94:95]
	s_waitcnt lgkmcnt(0)
	v_lshl_add_u64 v[94:95], s[10:11], 0, v[94:95]
	v_lshl_add_u64 v[94:95], v[94:95], 0, v[84:85]
	v_lshl_add_u64 v[102:103], v[94:95], 0, s[14:15]
	v_add_co_u32_e32 v94, vcc, s12, v94
	s_mov_b32 s10, 35
	s_nop 0
	v_addc_co_u32_e32 v95, vcc, 0, v95, vcc
	global_load_dword v107, v[94:95], off nt
	global_load_dword v104, v[102:103], off offset:256 nt
	global_load_dword v97, v[102:103], off offset:512 nt
	s_nop 0
	global_load_dword v94, v[102:103], off offset:768 nt
	s_ashr_i32 s11, s10, 31
	s_lshl_b64 s[10:11], s[10:11], 3
	s_add_u32 s10, s0, s10
	s_addc_u32 s11, s1, s11
	s_load_dwordx2 s[10:11], s[10:11], 0x0
	v_ashrrev_i32_e32 v103, 31, v27
	v_mov_b32_e32 v102, v27
	v_lshlrev_b64 v[102:103], 10, v[102:103]
	s_waitcnt lgkmcnt(0)
	v_lshl_add_u64 v[102:103], s[10:11], 0, v[102:103]
	v_lshl_add_u64 v[102:103], v[102:103], 0, v[84:85]
	v_lshl_add_u64 v[110:111], v[102:103], 0, s[14:15]
	v_add_co_u32_e32 v102, vcc, s12, v102
	s_mov_b32 s10, 35
	s_nop 0
	v_addc_co_u32_e32 v103, vcc, 0, v103, vcc
	global_load_dword v109, v[102:103], off nt
	global_load_dword v105, v[110:111], off offset:256 nt
	global_load_dword v101, v[110:111], off offset:512 nt
	global_load_dword v95, v[110:111], off offset:768 nt
	s_ashr_i32 s11, s10, 31
	s_lshl_b64 s[10:11], s[10:11], 3
	s_add_u32 s10, s0, s10
	s_addc_u32 s11, s1, s11
	s_load_dwordx2 s[10:11], s[10:11], 0x0
	v_ashrrev_i32_e32 v103, 31, v28
	v_mov_b32_e32 v102, v28
	v_lshlrev_b64 v[102:103], 10, v[102:103]
	s_waitcnt vmcnt(19)
	v_cvt_f32_fp8_sdwa v119, v121 src0_sel:BYTE_1
	s_waitcnt lgkmcnt(0)
	v_lshl_add_u64 v[102:103], s[10:11], 0, v[102:103]
	v_lshl_add_u64 v[102:103], v[102:103], 0, v[84:85]
	v_lshl_add_u64 v[114:115], v[102:103], 0, s[14:15]
	v_add_co_u32_e32 v102, vcc, s12, v102
	s_mov_b32 s10, 35
	s_nop 0
	v_addc_co_u32_e32 v103, vcc, 0, v103, vcc
	global_load_dword v110, v[102:103], off nt
	global_load_dword v106, v[114:115], off offset:256 nt
	s_nop 0
	global_load_dword v102, v[114:115], off offset:512 nt
	global_load_dword v96, v[114:115], off offset:768 nt
	s_ashr_i32 s11, s10, 31
	s_lshl_b64 s[10:11], s[10:11], 3
	s_add_u32 s10, s0, s10
	s_addc_u32 s11, s1, s11
	s_load_dwordx2 s[10:11], s[10:11], 0x0
	v_ashrrev_i32_e32 v115, 31, v29
	v_mov_b32_e32 v114, v29
	v_lshlrev_b64 v[114:115], 10, v[114:115]
	v_cvt_f32_fp8_sdwa v120, v121 src0_sel:BYTE_2
	s_waitcnt lgkmcnt(0)
	v_lshl_add_u64 v[114:115], s[10:11], 0, v[114:115]
	v_lshl_add_u64 v[114:115], v[114:115], 0, v[84:85]
	v_lshl_add_u64 v[116:117], v[114:115], 0, s[14:15]
	v_add_co_u32_e32 v114, vcc, s12, v114
	s_waitcnt vmcnt(19)
	v_cvt_f32_fp8_e32 v122, v125
	v_addc_co_u32_e32 v115, vcc, 0, v115, vcc
	global_load_dword v111, v[114:115], off nt
	global_load_dword v108, v[116:117], off offset:256 nt
	global_load_dword v103, v[116:117], off offset:512 nt
	global_load_dword v85, v[116:117], off offset:768 nt
	v_cvt_f32_fp8_e32 v114, v118
	v_cvt_f32_fp8_sdwa v115, v118 src0_sel:BYTE_1
	v_cvt_f32_fp8_sdwa v116, v118 src0_sel:BYTE_2
	v_cvt_f32_fp8_sdwa v117, v118 src0_sel:BYTE_3
	v_cvt_f32_fp8_e32 v118, v121
	v_cvt_f32_fp8_sdwa v121, v121 src0_sel:BYTE_3
	v_cvt_f32_fp8_sdwa v123, v125 src0_sel:BYTE_1
	v_cvt_f32_fp8_sdwa v124, v125 src0_sel:BYTE_2
	v_cvt_f32_fp8_sdwa v125, v125 src0_sel:BYTE_3
	s_waitcnt vmcnt(19)
	v_cvt_f32_fp8_e32 v126, v129
	v_cvt_f32_fp8_sdwa v127, v129 src0_sel:BYTE_1
	v_cvt_f32_fp8_sdwa v128, v129 src0_sel:BYTE_2
	v_cvt_f32_fp8_sdwa v129, v129 src0_sel:BYTE_3
	v_pk_fma_f32 v[114:115], v[22:23], v[114:115], 0 op_sel_hi:[0,1,0]
	v_pk_fma_f32 v[116:117], v[22:23], v[116:117], 0 op_sel_hi:[0,1,0]
	v_pk_fma_f32 v[116:117], v[22:23], v[120:121], v[116:117] op_sel:[1,0,0]
	v_pk_fma_f32 v[114:115], v[22:23], v[118:119], v[114:115] op_sel:[1,0,0]
	v_pk_fma_f32 v[116:117], v[24:25], v[124:125], v[116:117] op_sel_hi:[0,1,1]
	v_pk_fma_f32 v[114:115], v[24:25], v[122:123], v[114:115] op_sel_hi:[0,1,1]
	v_pk_fma_f32 v[118:119], v[24:25], v[128:129], v[116:117] op_sel:[1,0,0]
	v_pk_fma_f32 v[120:121], v[24:25], v[126:127], v[114:115] op_sel:[1,0,0]
	ds_read_b128 v[114:117], v140
	v_cvt_f32_fp8_e32 v122, v134
	v_cvt_f32_fp8_sdwa v123, v134 src0_sel:BYTE_1
	v_cvt_f32_fp8_sdwa v124, v134 src0_sel:BYTE_2
	v_cvt_f32_fp8_sdwa v125, v134 src0_sel:BYTE_3
	s_waitcnt lgkmcnt(0)
	v_pk_fma_f32 v[70:71], v[114:115], v[120:121], v[70:71]
	v_pk_fma_f32 v[72:73], v[116:117], v[118:119], v[72:73]
	v_cvt_f32_fp8_e32 v114, v130
	v_cvt_f32_fp8_sdwa v115, v130 src0_sel:BYTE_1
	v_cvt_f32_fp8_sdwa v116, v130 src0_sel:BYTE_2
	v_cvt_f32_fp8_sdwa v117, v130 src0_sel:BYTE_3
	v_cvt_f32_fp8_e32 v118, v132
	v_cvt_f32_fp8_sdwa v119, v132 src0_sel:BYTE_1
	v_cvt_f32_fp8_sdwa v120, v132 src0_sel:BYTE_2
	v_cvt_f32_fp8_sdwa v121, v132 src0_sel:BYTE_3
	s_waitcnt vmcnt(18)
	v_cvt_f32_fp8_e32 v126, v137
	v_cvt_f32_fp8_sdwa v127, v137 src0_sel:BYTE_1
	v_cvt_f32_fp8_sdwa v128, v137 src0_sel:BYTE_2
	v_cvt_f32_fp8_sdwa v129, v137 src0_sel:BYTE_3
	v_pk_fma_f32 v[114:115], v[22:23], v[114:115], 0 op_sel_hi:[0,1,0]
	v_pk_fma_f32 v[116:117], v[22:23], v[116:117], 0 op_sel_hi:[0,1,0]
	v_pk_fma_f32 v[116:117], v[22:23], v[120:121], v[116:117] op_sel:[1,0,0]
	v_pk_fma_f32 v[114:115], v[22:23], v[118:119], v[114:115] op_sel:[1,0,0]
	v_pk_fma_f32 v[116:117], v[24:25], v[124:125], v[116:117] op_sel_hi:[0,1,1]
	v_pk_fma_f32 v[114:115], v[24:25], v[122:123], v[114:115] op_sel_hi:[0,1,1]
	v_pk_fma_f32 v[118:119], v[24:25], v[128:129], v[116:117] op_sel:[1,0,0]
	v_pk_fma_f32 v[120:121], v[24:25], v[126:127], v[114:115] op_sel:[1,0,0]
	ds_read_b128 v[114:117], v140 offset:1024
	v_cvt_f32_fp8_e32 v122, v135
	v_cvt_f32_fp8_sdwa v123, v135 src0_sel:BYTE_1
	v_cvt_f32_fp8_sdwa v124, v135 src0_sel:BYTE_2
	v_cvt_f32_fp8_sdwa v125, v135 src0_sel:BYTE_3
	s_waitcnt lgkmcnt(0)
	v_pk_fma_f32 v[58:59], v[114:115], v[120:121], v[58:59]
	v_pk_fma_f32 v[60:61], v[116:117], v[118:119], v[60:61]
	v_cvt_f32_fp8_e32 v114, v131
	v_cvt_f32_fp8_sdwa v115, v131 src0_sel:BYTE_1
	v_cvt_f32_fp8_sdwa v116, v131 src0_sel:BYTE_2
	v_cvt_f32_fp8_sdwa v117, v131 src0_sel:BYTE_3
	v_cvt_f32_fp8_e32 v118, v133
	v_cvt_f32_fp8_sdwa v119, v133 src0_sel:BYTE_1
	v_cvt_f32_fp8_sdwa v120, v133 src0_sel:BYTE_2
	v_cvt_f32_fp8_sdwa v121, v133 src0_sel:BYTE_3
	s_waitcnt vmcnt(17)
	v_cvt_f32_fp8_e32 v126, v138
	v_cvt_f32_fp8_sdwa v127, v138 src0_sel:BYTE_1
	v_cvt_f32_fp8_sdwa v128, v138 src0_sel:BYTE_2
	v_cvt_f32_fp8_sdwa v129, v138 src0_sel:BYTE_3
	v_pk_fma_f32 v[114:115], v[22:23], v[114:115], 0 op_sel_hi:[0,1,0]
	v_pk_fma_f32 v[116:117], v[22:23], v[116:117], 0 op_sel_hi:[0,1,0]
	v_pk_fma_f32 v[116:117], v[22:23], v[120:121], v[116:117] op_sel:[1,0,0]
	v_pk_fma_f32 v[114:115], v[22:23], v[118:119], v[114:115] op_sel:[1,0,0]
	v_pk_fma_f32 v[116:117], v[24:25], v[124:125], v[116:117] op_sel_hi:[0,1,1]
	v_pk_fma_f32 v[114:115], v[24:25], v[122:123], v[114:115] op_sel_hi:[0,1,1]
	v_pk_fma_f32 v[118:119], v[24:25], v[128:129], v[116:117] op_sel:[1,0,0]
	v_pk_fma_f32 v[120:121], v[24:25], v[126:127], v[114:115] op_sel:[1,0,0]
	ds_read_b128 v[114:117], v140 offset:2048
	v_cvt_f32_fp8_sdwa v122, v136 src0_sel:BYTE_2
	v_cvt_f32_fp8_sdwa v123, v136 src0_sel:BYTE_3
	s_waitcnt vmcnt(16)
	v_cvt_f32_fp8_e32 v124, v139
	v_cvt_f32_fp8_sdwa v125, v139 src0_sel:BYTE_1
	s_waitcnt lgkmcnt(0)
	v_pk_fma_f32 v[54:55], v[114:115], v[120:121], v[54:55]
	v_pk_fma_f32 v[56:57], v[116:117], v[118:119], v[56:57]
	v_cvt_f32_fp8_e32 v114, v112
	v_cvt_f32_fp8_sdwa v115, v112 src0_sel:BYTE_1
	v_cvt_f32_fp8_sdwa v116, v112 src0_sel:BYTE_2
	v_cvt_f32_fp8_sdwa v117, v112 src0_sel:BYTE_3
	v_cvt_f32_fp8_e32 v118, v113
	v_cvt_f32_fp8_sdwa v119, v113 src0_sel:BYTE_1
	v_cvt_f32_fp8_sdwa v112, v113 src0_sel:BYTE_2
	v_cvt_f32_fp8_sdwa v113, v113 src0_sel:BYTE_3
	v_cvt_f32_fp8_e32 v120, v136
	v_cvt_f32_fp8_sdwa v121, v136 src0_sel:BYTE_1
	v_cvt_f32_fp8_sdwa v126, v139 src0_sel:BYTE_2
	v_cvt_f32_fp8_sdwa v127, v139 src0_sel:BYTE_3
	v_pk_fma_f32 v[114:115], v[22:23], v[114:115], 0 op_sel_hi:[0,1,0]
	v_pk_fma_f32 v[116:117], v[22:23], v[116:117], 0 op_sel_hi:[0,1,0]
	v_pk_fma_f32 v[112:113], v[22:23], v[112:113], v[116:117] op_sel:[1,0,0]
	v_pk_fma_f32 v[114:115], v[22:23], v[118:119], v[114:115] op_sel:[1,0,0]
	v_pk_fma_f32 v[112:113], v[24:25], v[122:123], v[112:113] op_sel_hi:[0,1,1]
	v_pk_fma_f32 v[114:115], v[24:25], v[120:121], v[114:115] op_sel_hi:[0,1,1]
	v_pk_fma_f32 v[116:117], v[24:25], v[126:127], v[112:113] op_sel:[1,0,0]
	v_pk_fma_f32 v[118:119], v[24:25], v[124:125], v[114:115] op_sel:[1,0,0]
	ds_read_b128 v[112:115], v140 offset:3072
	s_waitcnt vmcnt(7)
	v_cvt_f32_fp8_e32 v120, v110
	v_cvt_f32_fp8_sdwa v121, v110 src0_sel:BYTE_1
	v_cvt_f32_fp8_sdwa v122, v110 src0_sel:BYTE_2
	v_cvt_f32_fp8_sdwa v123, v110 src0_sel:BYTE_3
	s_waitcnt lgkmcnt(0)
	v_pk_fma_f32 v[42:43], v[112:113], v[118:119], v[42:43]
	v_pk_fma_f32 v[44:45], v[114:115], v[116:117], v[44:45]
	v_cvt_f32_fp8_e32 v112, v107
	v_cvt_f32_fp8_sdwa v113, v107 src0_sel:BYTE_1
	v_cvt_f32_fp8_sdwa v114, v107 src0_sel:BYTE_2
	v_cvt_f32_fp8_sdwa v115, v107 src0_sel:BYTE_3
	v_cvt_f32_fp8_e32 v116, v109
	v_cvt_f32_fp8_sdwa v117, v109 src0_sel:BYTE_1
	v_cvt_f32_fp8_sdwa v118, v109 src0_sel:BYTE_2
	v_cvt_f32_fp8_sdwa v119, v109 src0_sel:BYTE_3
	s_waitcnt vmcnt(3)
	v_cvt_f32_fp8_e32 v124, v111
	v_cvt_f32_fp8_sdwa v125, v111 src0_sel:BYTE_1
	v_cvt_f32_fp8_sdwa v110, v111 src0_sel:BYTE_2
	v_cvt_f32_fp8_sdwa v111, v111 src0_sel:BYTE_3
	v_pk_fma_f32 v[114:115], v[30:31], v[114:115], 0 op_sel_hi:[0,1,0]
	v_pk_fma_f32 v[112:113], v[30:31], v[112:113], 0 op_sel_hi:[0,1,0]
	v_pk_fma_f32 v[112:113], v[30:31], v[116:117], v[112:113] op_sel:[1,0,0]
	v_pk_fma_f32 v[114:115], v[30:31], v[118:119], v[114:115] op_sel:[1,0,0]
	v_lshl_add_u32 v126, v99, 12, v89
	v_pk_fma_f32 v[114:115], v[32:33], v[122:123], v[114:115] op_sel_hi:[0,1,1]
	v_pk_fma_f32 v[112:113], v[32:33], v[120:121], v[112:113] op_sel_hi:[0,1,1]
	v_pk_fma_f32 v[116:117], v[32:33], v[124:125], v[112:113] op_sel:[1,0,0]
	v_pk_fma_f32 v[114:115], v[32:33], v[110:111], v[114:115] op_sel:[1,0,0]
	ds_read_b128 v[110:113], v126
	v_cvt_f32_fp8_sdwa v118, v106 src0_sel:BYTE_2
	v_cvt_f32_fp8_sdwa v119, v106 src0_sel:BYTE_3
	s_waitcnt vmcnt(2)
	v_cvt_f32_fp8_sdwa v107, v108 src0_sel:BYTE_1
	v_cvt_f32_fp8_sdwa v120, v108 src0_sel:BYTE_2
	s_waitcnt lgkmcnt(0)
	v_pk_fma_f32 v[52:53], v[112:113], v[114:115], v[52:53]
	v_pk_fma_f32 v[50:51], v[110:111], v[116:117], v[50:51]
	v_cvt_f32_fp8_e32 v110, v104
	v_cvt_f32_fp8_sdwa v111, v104 src0_sel:BYTE_1
	v_cvt_f32_fp8_sdwa v112, v104 src0_sel:BYTE_2
	v_cvt_f32_fp8_sdwa v113, v104 src0_sel:BYTE_3
	v_cvt_f32_fp8_e32 v114, v105
	v_cvt_f32_fp8_sdwa v115, v105 src0_sel:BYTE_1
	v_cvt_f32_fp8_sdwa v104, v105 src0_sel:BYTE_2
	v_cvt_f32_fp8_sdwa v105, v105 src0_sel:BYTE_3
	v_cvt_f32_fp8_e32 v116, v106
	v_cvt_f32_fp8_sdwa v117, v106 src0_sel:BYTE_1
	v_cvt_f32_fp8_e32 v106, v108
	v_cvt_f32_fp8_sdwa v121, v108 src0_sel:BYTE_3
	v_pk_fma_f32 v[108:109], v[30:31], v[112:113], 0 op_sel_hi:[0,1,0]
	v_pk_fma_f32 v[110:111], v[30:31], v[110:111], 0 op_sel_hi:[0,1,0]
	v_pk_fma_f32 v[110:111], v[30:31], v[114:115], v[110:111] op_sel:[1,0,0]
	v_pk_fma_f32 v[104:105], v[30:31], v[104:105], v[108:109] op_sel:[1,0,0]
	v_pk_fma_f32 v[108:109], v[32:33], v[116:117], v[110:111] op_sel_hi:[0,1,1]
	v_pk_fma_f32 v[104:105], v[32:33], v[118:119], v[104:105] op_sel_hi:[0,1,1]
	v_pk_fma_f32 v[108:109], v[32:33], v[106:107], v[108:109] op_sel:[1,0,0]
	v_pk_fma_f32 v[110:111], v[32:33], v[120:121], v[104:105] op_sel:[1,0,0]
	ds_read_b128 v[104:107], v126 offset:1024
	v_cvt_f32_fp8_e32 v112, v102
	v_cvt_f32_fp8_sdwa v113, v102 src0_sel:BYTE_1
	v_cvt_f32_fp8_sdwa v114, v102 src0_sel:BYTE_2
	v_cvt_f32_fp8_sdwa v115, v102 src0_sel:BYTE_3
	s_waitcnt lgkmcnt(0)
	v_pk_fma_f32 v[48:49], v[106:107], v[110:111], v[48:49]
	v_pk_fma_f32 v[46:47], v[104:105], v[108:109], v[46:47]
	v_cvt_f32_fp8_e32 v104, v97
	v_cvt_f32_fp8_sdwa v105, v97 src0_sel:BYTE_1
	v_cvt_f32_fp8_sdwa v106, v97 src0_sel:BYTE_2
	v_cvt_f32_fp8_sdwa v107, v97 src0_sel:BYTE_3
	v_cvt_f32_fp8_e32 v108, v101
	v_cvt_f32_fp8_sdwa v109, v101 src0_sel:BYTE_1
	v_cvt_f32_fp8_sdwa v110, v101 src0_sel:BYTE_2
	v_cvt_f32_fp8_sdwa v111, v101 src0_sel:BYTE_3
	s_waitcnt vmcnt(1)
	v_cvt_f32_fp8_e32 v116, v103
	v_cvt_f32_fp8_sdwa v117, v103 src0_sel:BYTE_1
	v_cvt_f32_fp8_sdwa v102, v103 src0_sel:BYTE_2
	v_cvt_f32_fp8_sdwa v103, v103 src0_sel:BYTE_3
	v_pk_fma_f32 v[106:107], v[30:31], v[106:107], 0 op_sel_hi:[0,1,0]
	v_pk_fma_f32 v[104:105], v[30:31], v[104:105], 0 op_sel_hi:[0,1,0]
	v_pk_fma_f32 v[104:105], v[30:31], v[108:109], v[104:105] op_sel:[1,0,0]
	v_pk_fma_f32 v[106:107], v[30:31], v[110:111], v[106:107] op_sel:[1,0,0]
	v_pk_fma_f32 v[104:105], v[32:33], v[112:113], v[104:105] op_sel_hi:[0,1,1]
	v_pk_fma_f32 v[106:107], v[32:33], v[114:115], v[106:107] op_sel_hi:[0,1,1]
	v_pk_fma_f32 v[108:109], v[32:33], v[116:117], v[104:105] op_sel:[1,0,0]
	v_pk_fma_f32 v[106:107], v[32:33], v[102:103], v[106:107] op_sel:[1,0,0]
	ds_read_b128 v[102:105], v126 offset:2048
	v_cvt_f32_fp8_sdwa v110, v96 src0_sel:BYTE_2
	v_cvt_f32_fp8_sdwa v111, v96 src0_sel:BYTE_3
	s_waitcnt vmcnt(0)
	v_cvt_f32_fp8_sdwa v97, v85 src0_sel:BYTE_1
	v_cvt_f32_fp8_sdwa v112, v85 src0_sel:BYTE_2
	s_waitcnt lgkmcnt(0)
	v_pk_fma_f32 v[40:41], v[104:105], v[106:107], v[40:41]
	v_pk_fma_f32 v[38:39], v[102:103], v[108:109], v[38:39]
	v_cvt_f32_fp8_e32 v102, v94
	v_cvt_f32_fp8_sdwa v103, v94 src0_sel:BYTE_1
	v_cvt_f32_fp8_sdwa v104, v94 src0_sel:BYTE_2
	v_cvt_f32_fp8_sdwa v105, v94 src0_sel:BYTE_3
	v_cvt_f32_fp8_e32 v106, v95
	v_cvt_f32_fp8_sdwa v107, v95 src0_sel:BYTE_1
	v_cvt_f32_fp8_sdwa v94, v95 src0_sel:BYTE_2
	v_cvt_f32_fp8_sdwa v95, v95 src0_sel:BYTE_3
	v_cvt_f32_fp8_e32 v108, v96
	v_cvt_f32_fp8_sdwa v109, v96 src0_sel:BYTE_1
	v_cvt_f32_fp8_e32 v96, v85
	v_cvt_f32_fp8_sdwa v113, v85 src0_sel:BYTE_3
	v_pk_fma_f32 v[104:105], v[30:31], v[104:105], 0 op_sel_hi:[0,1,0]
	v_pk_fma_f32 v[102:103], v[30:31], v[102:103], 0 op_sel_hi:[0,1,0]
	v_pk_fma_f32 v[102:103], v[30:31], v[106:107], v[102:103] op_sel:[1,0,0]
	v_pk_fma_f32 v[94:95], v[30:31], v[94:95], v[104:105] op_sel:[1,0,0]
	v_pk_fma_f32 v[102:103], v[32:33], v[108:109], v[102:103] op_sel_hi:[0,1,1]
	v_pk_fma_f32 v[94:95], v[32:33], v[110:111], v[94:95] op_sel_hi:[0,1,1]
	v_pk_fma_f32 v[102:103], v[32:33], v[96:97], v[102:103] op_sel:[1,0,0]
	v_pk_fma_f32 v[104:105], v[32:33], v[112:113], v[94:95] op_sel:[1,0,0]
	ds_read_b128 v[94:97], v126 offset:3072
	v_cvt_pk_bf16_f32 v85, v70, v71
	v_cvt_pk_bf16_f32 v101, v72, v73
	v_mov_b32_e32 v106, v1
	v_mov_b32_e32 v107, v1
	s_waitcnt lgkmcnt(0)
	v_pk_fma_f32 v[36:37], v[96:97], v[104:105], v[36:37]
	v_cvt_pk_bf16_f32 v104, v58, v59
	v_pk_fma_f32 v[34:35], v[94:95], v[102:103], v[34:35]
	v_cvt_pk_bf16_f32 v105, v60, v61
	v_cndmask_b32_e64 v102, v85, v104, s[8:9]
	v_lshlrev_b64 v[96:97], 11, v[90:91]
	v_lshl_add_u64 v[94:95], s[18:19], 0, v[96:97]
	v_mov_b32_dpp v106, v102 quad_perm:[1,0,3,2] row_mask:0xf bank_mask:0xf
	v_cndmask_b32_e64 v102, v101, v105, s[8:9]
	v_cndmask_b32_e64 v104, v104, v106, s[8:9]
	v_mov_b32_e32 v112, v1
	v_mov_b32_dpp v107, v102 quad_perm:[1,0,3,2] row_mask:0xf bank_mask:0xf
	v_cndmask_b32_e64 v102, v106, v85, s[8:9]
	v_cndmask_b32_e64 v103, v107, v101, s[8:9]
	v_cndmask_b32_e64 v105, v105, v107, s[8:9]
	v_lshlrev_b32_e32 v106, 1, v86
	v_mov_b32_e32 v107, v1
	v_lshl_add_u64 v[108:109], v[94:95], 0, v[106:107]
	global_store_dwordx4 v[108:109], v[102:105], off
	v_cvt_pk_bf16_f32 v85, v54, v55
	v_cvt_pk_bf16_f32 v101, v56, v57
	v_cvt_pk_bf16_f32 v102, v42, v43
	v_cvt_pk_bf16_f32 v103, v44, v45
	v_cndmask_b32_e64 v104, v85, v102, s[8:9]
	v_mov_b32_e32 v105, v1
	v_mov_b32_e32 v108, v1
	v_mov_b32_e32 v109, v1
	v_mov_b32_dpp v105, v104 quad_perm:[1,0,3,2] row_mask:0xf bank_mask:0xf
	v_cndmask_b32_e64 v104, v101, v103, s[8:9]
	v_mov_b32_e32 v113, v1
	s_nop 0
	v_mov_b32_dpp v108, v104 quad_perm:[1,0,3,2] row_mask:0xf bank_mask:0xf
	v_cndmask_b32_e64 v104, v102, v105, s[8:9]
	v_cndmask_b32_e64 v102, v105, v85, s[8:9]
	v_cndmask_b32_e64 v105, v103, v108, s[8:9]
	v_cndmask_b32_e64 v103, v108, v101, s[8:9]
	v_lshlrev_b32_e32 v108, 1, v88
	v_lshl_add_u64 v[94:95], v[94:95], 0, v[108:109]
	global_store_dwordx4 v[94:95], v[102:105], off
	v_cvt_pk_bf16_f32 v85, v50, v51
	v_cvt_pk_bf16_f32 v101, v52, v53
	v_cvt_pk_bf16_f32 v104, v46, v47
	v_cvt_pk_bf16_f32 v105, v48, v49
	v_cndmask_b32_e64 v102, v85, v104, s[8:9]
	v_lshlrev_b64 v[94:95], 11, v[92:93]
	v_lshl_add_u64 v[110:111], s[18:19], 0, v[94:95]
	v_mov_b32_dpp v112, v102 quad_perm:[1,0,3,2] row_mask:0xf bank_mask:0xf
	v_cndmask_b32_e64 v102, v101, v105, s[8:9]
	v_cndmask_b32_e64 v104, v104, v112, s[8:9]
	v_lshl_add_u64 v[106:107], v[110:111], 0, v[106:107]
	v_mov_b32_dpp v113, v102 quad_perm:[1,0,3,2] row_mask:0xf bank_mask:0xf
	v_cndmask_b32_e64 v103, v113, v101, s[8:9]
	v_cndmask_b32_e64 v102, v112, v85, s[8:9]
	v_cndmask_b32_e64 v105, v105, v113, s[8:9]
	global_store_dwordx4 v[106:107], v[102:105], off
	v_cvt_pk_bf16_f32 v85, v38, v39
	v_cvt_pk_bf16_f32 v101, v40, v41
	v_cvt_pk_bf16_f32 v102, v34, v35
	v_cvt_pk_bf16_f32 v103, v36, v37
	v_cndmask_b32_e64 v104, v85, v102, s[8:9]
	v_mov_b32_e32 v106, v1
	v_mov_b32_e32 v107, v1
	s_nop 0
	v_mov_b32_dpp v106, v104 quad_perm:[1,0,3,2] row_mask:0xf bank_mask:0xf
	v_cndmask_b32_e64 v104, v101, v103, s[8:9]
	s_nop 1
	v_mov_b32_dpp v107, v104 quad_perm:[1,0,3,2] row_mask:0xf bank_mask:0xf
	v_cndmask_b32_e64 v105, v103, v107, s[8:9]
	v_cndmask_b32_e64 v104, v102, v106, s[8:9]
	v_cndmask_b32_e64 v103, v107, v101, s[8:9]
	v_cndmask_b32_e64 v102, v106, v85, s[8:9]
	v_lshl_add_u64 v[106:107], v[110:111], 0, v[108:109]
	global_store_dwordx4 v[106:107], v[102:105], off
	s_cbranch_execnz .LBB0_368
	s_branch .LBB0_367

.LBB0_1977:
	v_ashrrev_i32_e32 v66, 12, v72
	v_and_b32_e32 v67, 0xffc, v72
	s_waitcnt vmcnt(7)
	v_ashrrev_i32_e32 v49, 31, v44
	v_mov_b32_e32 v48, v44
	v_ashrrev_i32_e32 v51, 31, v45
	v_mov_b32_e32 v50, v45
	v_ashrrev_i32_e32 v45, 31, v46
	v_mov_b32_e32 v44, v46
	v_ashrrev_i32_e32 v53, 31, v47
	v_mov_b32_e32 v52, v47
	s_waitcnt vmcnt(5)
	v_ashrrev_i32_e32 v47, 31, v40
	v_mov_b32_e32 v46, v40
	v_ashrrev_i32_e32 v55, 31, v41
	v_mov_b32_e32 v54, v41
	v_ashrrev_i32_e32 v41, 31, v42
	v_mov_b32_e32 v40, v42
	v_ashrrev_i32_e32 v57, 31, v43
	v_mov_b32_e32 v56, v43
	s_waitcnt vmcnt(3)
	v_ashrrev_i32_e32 v43, 31, v32
	v_mov_b32_e32 v42, v32
	v_ashrrev_i32_e32 v59, 31, v33
	v_mov_b32_e32 v58, v33
	v_ashrrev_i32_e32 v33, 31, v34
	v_mov_b32_e32 v32, v34
	v_mad_i32_i24 v82, v66, s47, v67
	v_add_u32_e32 v80, s78, v72
	v_ashrrev_i32_e32 v61, 31, v35
	v_mov_b32_e32 v60, v35
	s_waitcnt vmcnt(0)
	v_ashrrev_i32_e32 v35, 31, v36
	v_mov_b32_e32 v34, v36
	v_ashrrev_i32_e32 v63, 31, v37
	v_mov_b32_e32 v62, v37
	v_ashrrev_i32_e32 v37, 31, v38
	v_mov_b32_e32 v36, v38
	v_lshlrev_b64 v[116:117], 10, v[32:33]
	v_ashrrev_i32_e32 v83, 31, v82
	v_or_b32_e32 v32, 1, v82
	v_cmp_gt_i32_e64 s[2:3], s71, v80
	v_lshlrev_b64 v[156:157], 10, v[40:41]
	v_lshlrev_b64 v[70:71], 10, v[34:35]
	v_lshlrev_b64 v[66:67], 10, v[36:37]
	v_or_b32_e32 v34, 2, v82
	v_or_b32_e32 v36, 3, v82
	v_lshlrev_b64 v[40:41], 11, v[82:83]
	v_ashrrev_i32_e32 v33, 31, v32
	v_ashrrev_i32_e32 v65, 31, v39
	v_mov_b32_e32 v64, v39
	v_and_b32_e32 v81, 0xfffff000, v72
	v_cndmask_b32_e64 v86, v72, v80, s[2:3]
	v_ashrrev_i32_e32 v35, 31, v34
	v_ashrrev_i32_e32 v37, 31, v36
	v_lshl_add_u64 v[40:41], v[76:77], 0, v[40:41]
	v_lshlrev_b64 v[32:33], 11, v[32:33]
	v_cmp_lt_i32_e32 vcc, s70, v80
	v_lshlrev_b64 v[152:153], 10, v[42:43]
	v_lshlrev_b64 v[96:97], 10, v[64:65]
	v_add_u32_e32 v168, v167, v81
	v_mov_b32_e32 v72, v80
	v_ashrrev_i32_e32 v42, 12, v86
	v_and_b32_e32 v43, 0xffc, v86
	v_lshlrev_b64 v[34:35], 11, v[34:35]
	v_lshlrev_b64 v[36:37], 11, v[36:37]
	global_load_dwordx2 v[64:65], v[40:41], off
	global_load_dwordx2 v[80:81], v[40:41], off offset:512
	global_load_dwordx2 v[82:83], v[40:41], off offset:1024
	global_load_dwordx2 v[86:87], v[40:41], off offset:1536
	v_lshl_add_u64 v[32:33], v[76:77], 0, v[32:33]
	s_mov_b32 s10, 35
	v_lshl_add_u64 v[34:35], v[76:77], 0, v[34:35]
	v_lshl_add_u64 v[36:37], v[76:77], 0, v[36:37]
	global_load_dwordx2 v[88:89], v[32:33], off
	global_load_dwordx2 v[90:91], v[32:33], off offset:512
	global_load_dwordx2 v[92:93], v[32:33], off offset:1024
	global_load_dwordx2 v[94:95], v[32:33], off offset:1536
	global_load_dwordx2 v[100:101], v[34:35], off
	global_load_dwordx2 v[104:105], v[34:35], off offset:512
	global_load_dwordx2 v[108:109], v[34:35], off offset:1024
	global_load_dwordx2 v[112:113], v[34:35], off offset:1536
	global_load_dwordx2 v[174:175], v[36:37], off
	global_load_dwordx2 v[176:177], v[36:37], off offset:512
	global_load_dwordx2 v[178:179], v[36:37], off offset:1024
	global_load_dwordx2 v[180:181], v[36:37], off offset:1536
	s_ashr_i32 s11, s10, 31
	s_lshl_b64 s[2:3], s[10:11], 3
	s_add_u32 s2, s0, s2
	s_mov_b32 s14, 35
	s_addc_u32 s3, s1, s3
	s_load_dwordx2 s[2:3], s[2:3], 0x0
	s_ashr_i32 s15, s14, 31
	s_lshl_b64 s[10:11], s[14:15], 3
	s_add_u32 s10, s0, s10
	v_mul_i32_i24_e32 v42, 0x1100, v42
	s_addc_u32 s11, s1, s11
	v_add_lshl_u32 v42, v42, v43, 2
	s_load_dwordx2 s[10:11], s[10:11], 0x0
	v_ashrrev_i32_e32 v43, 31, v42
	v_or_b32_e32 v40, 4, v42
	v_lshlrev_b64 v[32:33], 2, v[42:43]
	v_ashrrev_i32_e32 v41, 31, v40
	v_lshlrev_b64 v[34:35], 2, v[40:41]
	s_waitcnt lgkmcnt(0)
	v_lshl_add_u64 v[40:41], s[2:3], 0, v[32:33]
	v_add_co_u32_e64 v40, s[2:3], s33, v40
	v_lshl_add_u64 v[32:33], s[10:11], 0, v[32:33]
	s_nop 0
	v_addc_co_u32_e64 v41, s[2:3], 0, v41, s[2:3]
	v_lshlrev_b64 v[162:163], 10, v[44:45]
	v_lshlrev_b64 v[158:159], 10, v[46:47]
	v_or_b32_e32 v44, 8, v42
	v_or_b32_e32 v46, 12, v42
	v_add_co_u32_e64 v32, s[2:3], s46, v32
	s_mov_b32 s18, 35
	v_ashrrev_i32_e32 v45, 31, v44
	v_ashrrev_i32_e32 v47, 31, v46
	v_addc_co_u32_e64 v33, s[2:3], 0, v33, s[2:3]
	v_lshlrev_b64 v[84:85], 10, v[48:49]
	v_lshlrev_b64 v[114:115], 10, v[60:61]
	v_lshlrev_b64 v[68:69], 10, v[62:63]
	v_lshlrev_b64 v[36:37], 2, v[44:45]
	v_lshlrev_b64 v[48:49], 2, v[46:47]
	global_load_dwordx4 v[44:47], v[40:41], off
	global_load_dwordx4 v[60:63], v[32:33], off
	s_ashr_i32 s19, s18, 31
	s_lshl_b64 s[2:3], s[18:19], 3
	s_add_u32 s2, s0, s2
	s_mov_b32 s22, 35
	s_addc_u32 s3, s1, s3
	s_load_dwordx2 s[2:3], s[2:3], 0x0
	s_ashr_i32 s23, s22, 31
	s_lshl_b64 s[10:11], s[22:23], 3
	s_add_u32 s10, s0, s10
	s_addc_u32 s11, s1, s11
	s_load_dwordx2 s[10:11], s[10:11], 0x0
	s_waitcnt lgkmcnt(0)
	v_lshl_add_u64 v[32:33], s[2:3], 0, v[34:35]
	v_add_co_u32_e64 v32, s[2:3], s33, v32
	s_mov_b32 s26, 35
	s_nop 0
	v_addc_co_u32_e64 v33, s[2:3], 0, v33, s[2:3]
	global_load_dwordx4 v[40:43], v[32:33], off
	v_lshl_add_u64 v[32:33], s[10:11], 0, v[34:35]
	v_add_co_u32_e64 v32, s[2:3], s46, v32
	v_lshlrev_b64 v[154:155], 10, v[56:57]
	s_nop 0
	v_addc_co_u32_e64 v33, s[2:3], 0, v33, s[2:3]
	v_lshlrev_b64 v[150:151], 10, v[58:59]
	global_load_dwordx4 v[56:59], v[32:33], off
	s_ashr_i32 s27, s26, 31
	s_lshl_b64 s[2:3], s[26:27], 3
	s_add_u32 s2, s0, s2
	s_mov_b32 s36, 35
	s_addc_u32 s3, s1, s3
	s_load_dwordx2 s[2:3], s[2:3], 0x0
	s_ashr_i32 s37, s36, 31
	s_lshl_b64 s[10:11], s[36:37], 3
	s_add_u32 s10, s0, s10
	s_addc_u32 s11, s1, s11
	s_load_dwordx2 s[10:11], s[10:11], 0x0
	s_waitcnt lgkmcnt(0)
	v_lshl_add_u64 v[32:33], s[2:3], 0, v[36:37]
	v_add_co_u32_e64 v32, s[2:3], s33, v32
	s_mov_b32 s42, 35
	s_nop 0
	v_addc_co_u32_e64 v33, s[2:3], 0, v33, s[2:3]
	v_lshl_add_u64 v[36:37], s[10:11], 0, v[36:37]
	v_add_co_u32_e64 v36, s[2:3], s46, v36
	v_lshlrev_b64 v[160:161], 10, v[52:53]
	s_nop 0
	v_addc_co_u32_e64 v37, s[2:3], 0, v37, s[2:3]
	v_lshlrev_b64 v[38:39], 10, v[54:55]
	global_load_dwordx4 v[32:35], v[32:33], off
	s_mov_b32 s52, 35
	global_load_dwordx4 v[52:55], v[36:37], off
	s_ashr_i32 s43, s42, 31
	s_lshl_b64 s[2:3], s[42:43], 3
	s_add_u32 s2, s0, s2
	s_addc_u32 s3, s1, s3
	s_load_dwordx2 s[2:3], s[2:3], 0x0
	s_ashr_i32 s53, s52, 31
	s_lshl_b64 s[10:11], s[52:53], 3
	s_add_u32 s10, s0, s10
	s_addc_u32 s11, s1, s11
	s_load_dwordx2 s[10:11], s[10:11], 0x0
	s_waitcnt lgkmcnt(0)
	v_lshl_add_u64 v[36:37], s[2:3], 0, v[48:49]
	v_add_co_u32_e64 v36, s[2:3], s33, v36
	s_mov_b32 s58, 35
	s_nop 0
	v_addc_co_u32_e64 v37, s[2:3], 0, v37, s[2:3]
	global_load_dwordx4 v[170:173], v[36:37], off
	v_lshl_add_u64 v[36:37], s[10:11], 0, v[48:49]
	v_add_co_u32_e64 v36, s[2:3], s46, v36
	v_lshlrev_b64 v[164:165], 10, v[50:51]
	s_nop 0
	v_addc_co_u32_e64 v37, s[2:3], 0, v37, s[2:3]
	global_load_dwordx4 v[48:51], v[36:37], off
	s_ashr_i32 s59, s58, 31
	s_lshl_b64 s[2:3], s[58:59], 3
	s_add_u32 s2, s0, s2
	s_addc_u32 s3, s1, s3
	s_load_dwordx2 s[2:3], s[2:3], 0x0
	v_lshlrev_b32_e32 v74, 2, v166
	s_waitcnt vmcnt(23)
	v_lshlrev_b32_e32 v118, 16, v64
	v_and_b32_e32 v119, 0xffff0000, v64
	v_lshlrev_b32_e32 v122, 16, v65
	s_waitcnt lgkmcnt(0)
	v_lshl_add_u64 v[36:37], s[2:3], 0, v[84:85]
	v_lshl_add_u64 v[36:37], v[36:37], 0, v[74:75]
	v_and_b32_e32 v123, 0xffff0000, v65
	v_lshl_add_u64 v[64:65], v[36:37], 0, s[8:9]
	v_add_co_u32_e64 v36, s[2:3], s72, v36
	s_mov_b32 s28, 35
	s_nop 0
	v_addc_co_u32_e64 v37, s[2:3], 0, v37, s[2:3]
	s_waitcnt vmcnt(22)
	v_lshlrev_b32_e32 v120, 16, v80
	v_and_b32_e32 v121, 0xffff0000, v80
	v_lshlrev_b32_e32 v126, 16, v81
	v_and_b32_e32 v127, 0xffff0000, v81
	s_waitcnt vmcnt(21)
	v_lshlrev_b32_e32 v124, 16, v82
	v_and_b32_e32 v125, 0xffff0000, v82
	v_lshlrev_b32_e32 v130, 16, v83
	v_and_b32_e32 v131, 0xffff0000, v83
	s_waitcnt vmcnt(11)
	v_lshlrev_b32_e32 v80, 16, v174
	v_and_b32_e32 v81, 0xffff0000, v174
	v_lshlrev_b32_e32 v82, 16, v175
	v_and_b32_e32 v83, 0xffff0000, v175
	s_waitcnt vmcnt(10)
	v_lshlrev_b32_e32 v84, 16, v176
	v_and_b32_e32 v85, 0xffff0000, v176
	global_load_dword v169, v[36:37], off nt
	global_load_dword v174, v[64:65], off offset:256 nt
	global_load_dword v175, v[64:65], off offset:512 nt
	global_load_dword v176, v[64:65], off offset:768 nt
	s_ashr_i32 s29, s28, 31
	s_lshl_b64 s[2:3], s[28:29], 3
	s_add_u32 s2, s0, s2
	s_addc_u32 s3, s1, s3
	s_load_dwordx2 s[2:3], s[2:3], 0x0
	s_mov_b32 s34, 35
	v_lshlrev_b32_e32 v132, 16, v88
	v_and_b32_e32 v133, 0xffff0000, v88
	v_lshlrev_b32_e32 v138, 16, v89
	s_waitcnt lgkmcnt(0)
	v_lshl_add_u64 v[36:37], s[2:3], 0, v[164:165]
	v_lshl_add_u64 v[36:37], v[36:37], 0, v[74:75]
	v_lshl_add_u64 v[64:65], v[36:37], 0, s[8:9]
	v_add_co_u32_e64 v36, s[2:3], s72, v36
	v_and_b32_e32 v139, 0xffff0000, v89
	s_nop 0
	v_addc_co_u32_e64 v37, s[2:3], 0, v37, s[2:3]
	v_lshlrev_b32_e32 v140, 16, v92
	v_and_b32_e32 v141, 0xffff0000, v92
	v_lshlrev_b32_e32 v146, 16, v93
	v_and_b32_e32 v147, 0xffff0000, v93
	v_lshlrev_b32_e32 v88, 16, v177
	v_and_b32_e32 v89, 0xffff0000, v177
	s_waitcnt vmcnt(13)
	v_lshlrev_b32_e32 v92, 16, v179
	v_and_b32_e32 v93, 0xffff0000, v179
	global_load_dword v177, v[36:37], off nt
	global_load_dword v179, v[64:65], off offset:256 nt
	global_load_dword v183, v[64:65], off offset:512 nt
	global_load_dword v187, v[64:65], off offset:768 nt
	s_ashr_i32 s35, s34, 31
	s_lshl_b64 s[2:3], s[34:35], 3
	s_add_u32 s2, s0, s2
	s_addc_u32 s3, s1, s3
	s_load_dwordx2 s[2:3], s[2:3], 0x0
	s_mov_b32 s38, 35
	s_mov_b32 s44, 35
	s_mov_b32 s50, 35
	s_mov_b32 s56, 35
	s_waitcnt lgkmcnt(0)
	v_lshl_add_u64 v[36:37], s[2:3], 0, v[162:163]
	v_lshl_add_u64 v[36:37], v[36:37], 0, v[74:75]
	v_lshl_add_u64 v[64:65], v[36:37], 0, s[8:9]
	v_add_co_u32_e64 v36, s[2:3], s72, v36
	s_mov_b32 s60, 35
	s_nop 0
	v_addc_co_u32_e64 v37, s[2:3], 0, v37, s[2:3]
	global_load_dword v188, v[36:37], off nt
	global_load_dword v189, v[64:65], off offset:256 nt
	global_load_dword v190, v[64:65], off offset:512 nt
	global_load_dword v191, v[64:65], off offset:768 nt
	s_ashr_i32 s39, s38, 31
	s_lshl_b64 s[2:3], s[38:39], 3
	s_add_u32 s2, s0, s2
	s_addc_u32 s3, s1, s3
	s_load_dwordx2 s[2:3], s[2:3], 0x0
	s_mov_b32 s54, 35
	v_lshlrev_b32_e32 v128, 16, v86
	v_and_b32_e32 v129, 0xffff0000, v86
	v_lshlrev_b32_e32 v134, 16, v87
	s_waitcnt lgkmcnt(0)
	v_lshl_add_u64 v[36:37], s[2:3], 0, v[160:161]
	v_lshl_add_u64 v[36:37], v[36:37], 0, v[74:75]
	v_lshl_add_u64 v[64:65], v[36:37], 0, s[8:9]
	v_add_co_u32_e64 v36, s[2:3], s72, v36
	v_and_b32_e32 v135, 0xffff0000, v87
	s_nop 0
	v_addc_co_u32_e64 v37, s[2:3], 0, v37, s[2:3]
	global_load_dword v192, v[36:37], off nt
	global_load_dword v193, v[64:65], off offset:256 nt
	global_load_dword v194, v[64:65], off offset:512 nt
	global_load_dword v195, v[64:65], off offset:768 nt
	s_ashr_i32 s45, s44, 31
	s_lshl_b64 s[2:3], s[44:45], 3
	s_add_u32 s2, s0, s2
	s_addc_u32 s3, s1, s3
	s_load_dwordx2 s[2:3], s[2:3], 0x0
	v_lshlrev_b32_e32 v136, 16, v90
	v_and_b32_e32 v137, 0xffff0000, v90
	v_lshlrev_b32_e32 v142, 16, v91
	v_and_b32_e32 v143, 0xffff0000, v91
	s_waitcnt lgkmcnt(0)
	v_lshl_add_u64 v[36:37], s[2:3], 0, v[158:159]
	v_lshl_add_u64 v[36:37], v[36:37], 0, v[74:75]
	v_lshl_add_u64 v[64:65], v[36:37], 0, s[8:9]
	v_add_co_u32_e64 v36, s[2:3], s72, v36
	s_waitcnt vmcnt(14)
	v_cvt_f32_fp8_sdwa v160, v174 src0_sel:BYTE_2
	v_addc_co_u32_e64 v37, s[2:3], 0, v37, s[2:3]
	global_load_dword v196, v[36:37], off nt
	global_load_dword v197, v[64:65], off offset:256 nt
	global_load_dword v198, v[64:65], off offset:512 nt
	global_load_dword v199, v[64:65], off offset:768 nt
	s_ashr_i32 s51, s50, 31
	s_lshl_b64 s[2:3], s[50:51], 3
	s_add_u32 s2, s0, s2
	s_addc_u32 s3, s1, s3
	s_load_dwordx2 s[2:3], s[2:3], 0x0
	v_cvt_f32_fp8_sdwa v161, v174 src0_sel:BYTE_3
	s_waitcnt vmcnt(17)
	v_cvt_f32_fp8_e32 v162, v175
	v_cvt_f32_fp8_sdwa v163, v175 src0_sel:BYTE_1
	v_cvt_f32_fp8_sdwa v164, v175 src0_sel:BYTE_2
	s_waitcnt lgkmcnt(0)
	v_lshl_add_u64 v[64:65], s[2:3], 0, v[38:39]
	v_lshl_add_u64 v[64:65], v[64:65], 0, v[74:75]
	v_lshl_add_u64 v[158:159], v[64:65], 0, s[8:9]
	v_add_co_u32_e64 v64, s[2:3], s72, v64
	v_cvt_f32_fp8_sdwa v165, v175 src0_sel:BYTE_3
	s_nop 0
	v_addc_co_u32_e64 v65, s[2:3], 0, v65, s[2:3]
	global_load_dword v200, v[64:65], off nt
	global_load_dword v201, v[158:159], off offset:256 nt
	global_load_dword v202, v[158:159], off offset:512 nt
	global_load_dword v203, v[158:159], off offset:768 nt
	s_ashr_i32 s57, s56, 31
	s_lshl_b64 s[2:3], s[56:57], 3
	s_add_u32 s2, s0, s2
	s_addc_u32 s3, s1, s3
	s_load_dwordx2 s[2:3], s[2:3], 0x0
	v_cvt_f32_fp8_e32 v158, v174
	v_cvt_f32_fp8_sdwa v159, v174 src0_sel:BYTE_1
	v_mov_b64_e32 v[36:37], v[170:171]
	v_mov_b64_e32 v[38:39], v[172:173]
	s_waitcnt lgkmcnt(0)
	v_lshl_add_u64 v[64:65], s[2:3], 0, v[156:157]
	v_lshl_add_u64 v[64:65], v[64:65], 0, v[74:75]
	v_lshl_add_u64 v[156:157], v[64:65], 0, s[8:9]
	v_add_co_u32_e64 v64, s[2:3], s72, v64
	s_waitcnt vmcnt(20)
	v_cvt_f32_fp8_e32 v170, v176
	v_addc_co_u32_e64 v65, s[2:3], 0, v65, s[2:3]
	global_load_dword v204, v[64:65], off nt
	global_load_dword v205, v[156:157], off offset:256 nt
	global_load_dword v206, v[156:157], off offset:512 nt
	global_load_dword v207, v[156:157], off offset:768 nt
	s_ashr_i32 s61, s60, 31
	s_lshl_b64 s[2:3], s[60:61], 3
	s_add_u32 s2, s0, s2
	s_addc_u32 s3, s1, s3
	s_load_dwordx2 s[2:3], s[2:3], 0x0
	v_cvt_f32_fp8_e32 v64, v169
	v_cvt_f32_fp8_sdwa v65, v169 src0_sel:BYTE_1
	v_cvt_f32_fp8_sdwa v156, v169 src0_sel:BYTE_2
	v_cvt_f32_fp8_sdwa v157, v169 src0_sel:BYTE_3
	s_waitcnt lgkmcnt(0)
	v_lshl_add_u64 v[154:155], s[2:3], 0, v[154:155]
	v_lshl_add_u64 v[154:155], v[154:155], 0, v[74:75]
	v_lshl_add_u64 v[174:175], v[154:155], 0, s[8:9]
	v_add_co_u32_e64 v154, s[2:3], s72, v154
	v_cvt_f32_fp8_sdwa v171, v176 src0_sel:BYTE_1
	s_nop 0
	v_addc_co_u32_e64 v155, s[2:3], 0, v155, s[2:3]
	global_load_dword v169, v[154:155], off nt
	global_load_dword v208, v[174:175], off offset:256 nt
	global_load_dword v209, v[174:175], off offset:512 nt
	global_load_dword v210, v[174:175], off offset:768 nt
	s_ashr_i32 s55, s54, 31
	s_lshl_b64 s[2:3], s[54:55], 3
	s_add_u32 s2, s0, s2
	s_addc_u32 s3, s1, s3
	v_cvt_f32_fp8_sdwa v172, v176 src0_sel:BYTE_2
	v_cvt_f32_fp8_sdwa v173, v176 src0_sel:BYTE_3
	s_load_dwordx2 s[2:3], s[2:3], 0x0
	v_lshlrev_b32_e32 v144, 16, v94
	v_and_b32_e32 v145, 0xffff0000, v94
	v_lshlrev_b32_e32 v148, 16, v95
	v_and_b32_e32 v149, 0xffff0000, v95
	v_lshlrev_b32_e32 v86, 16, v178
	v_and_b32_e32 v87, 0xffff0000, v178
	v_lshlrev_b32_e32 v90, 16, v180
	v_and_b32_e32 v91, 0xffff0000, v180
	v_lshlrev_b32_e32 v94, 16, v181
	v_and_b32_e32 v95, 0xffff0000, v181
	s_waitcnt vmcnt(27)
	v_cvt_f32_fp8_e32 v154, v177
	v_cvt_f32_fp8_sdwa v155, v177 src0_sel:BYTE_1
	v_cvt_f32_fp8_sdwa v174, v177 src0_sel:BYTE_2
	v_cvt_f32_fp8_sdwa v175, v177 src0_sel:BYTE_3
	s_waitcnt vmcnt(26)
	v_cvt_f32_fp8_e32 v176, v179
	v_cvt_f32_fp8_sdwa v177, v179 src0_sel:BYTE_1
	v_cvt_f32_fp8_sdwa v178, v179 src0_sel:BYTE_2
	v_cvt_f32_fp8_sdwa v179, v179 src0_sel:BYTE_3
	s_waitcnt vmcnt(25)
	v_cvt_f32_fp8_e32 v180, v183
	v_cvt_f32_fp8_sdwa v181, v183 src0_sel:BYTE_1
	v_cvt_f32_fp8_sdwa v182, v183 src0_sel:BYTE_2
	v_cvt_f32_fp8_sdwa v183, v183 src0_sel:BYTE_3
	s_waitcnt vmcnt(24)
	v_cvt_f32_fp8_e32 v184, v187
	v_cvt_f32_fp8_sdwa v185, v187 src0_sel:BYTE_1
	v_cvt_f32_fp8_sdwa v186, v187 src0_sel:BYTE_2
	v_cvt_f32_fp8_sdwa v187, v187 src0_sel:BYTE_3
	v_pk_fma_f32 v[156:157], v[16:17], v[156:157], 0 op_sel_hi:[0,1,0]
	v_pk_fma_f32 v[64:65], v[16:17], v[64:65], 0 op_sel_hi:[0,1,0]
	v_pk_fma_f32 v[160:161], v[16:17], v[160:161], 0 op_sel_hi:[0,1,0]
	v_pk_fma_f32 v[158:159], v[16:17], v[158:159], 0 op_sel_hi:[0,1,0]
	v_pk_fma_f32 v[164:165], v[16:17], v[164:165], 0 op_sel_hi:[0,1,0]
	v_pk_fma_f32 v[162:163], v[16:17], v[162:163], 0 op_sel_hi:[0,1,0]
	v_pk_fma_f32 v[172:173], v[16:17], v[172:173], 0 op_sel_hi:[0,1,0]
	v_pk_fma_f32 v[170:171], v[16:17], v[170:171], 0 op_sel_hi:[0,1,0]
	v_pk_fma_f32 v[64:65], v[16:17], v[154:155], v[64:65] op_sel:[1,0,0]
	v_pk_fma_f32 v[154:155], v[16:17], v[174:175], v[156:157] op_sel:[1,0,0]
	v_pk_fma_f32 v[156:157], v[16:17], v[176:177], v[158:159] op_sel:[1,0,0]
	v_pk_fma_f32 v[158:159], v[16:17], v[178:179], v[160:161] op_sel:[1,0,0]
	v_pk_fma_f32 v[160:161], v[16:17], v[180:181], v[162:163] op_sel:[1,0,0]
	v_pk_fma_f32 v[162:163], v[16:17], v[182:183], v[164:165] op_sel:[1,0,0]
	v_pk_fma_f32 v[164:165], v[16:17], v[184:185], v[170:171] op_sel:[1,0,0]
	v_pk_fma_f32 v[170:171], v[16:17], v[186:187], v[172:173] op_sel:[1,0,0]
	v_mov_b64_e32 v[16:17], v[60:61]
	s_waitcnt lgkmcnt(0)
	v_lshl_add_u64 v[60:61], s[2:3], 0, v[152:153]
	v_lshl_add_u64 v[60:61], v[60:61], 0, v[74:75]
	v_lshl_add_u64 v[152:153], v[60:61], 0, s[8:9]
	v_add_co_u32_e64 v60, s[2:3], s72, v60
	s_mov_b32 s48, 35
	s_nop 0
	v_addc_co_u32_e64 v61, s[2:3], 0, v61, s[2:3]
	global_load_dword v211, v[60:61], off nt
	global_load_dword v212, v[152:153], off offset:256 nt
	global_load_dword v213, v[152:153], off offset:512 nt
	global_load_dword v214, v[152:153], off offset:768 nt
	s_ashr_i32 s49, s48, 31
	s_lshl_b64 s[2:3], s[48:49], 3
	s_add_u32 s2, s0, s2
	s_addc_u32 s3, s1, s3
	s_load_dwordx2 s[2:3], s[2:3], 0x0
	s_waitcnt vmcnt(27)
	v_cvt_f32_fp8_sdwa v152, v188 src0_sel:BYTE_2
	v_cvt_f32_fp8_sdwa v153, v188 src0_sel:BYTE_3
	s_waitcnt vmcnt(26)
	v_cvt_f32_fp8_e32 v172, v189
	v_cvt_f32_fp8_sdwa v173, v189 src0_sel:BYTE_1
	s_waitcnt vmcnt(25)
	v_cvt_f32_fp8_sdwa v178, v190 src0_sel:BYTE_2
	v_cvt_f32_fp8_sdwa v179, v190 src0_sel:BYTE_3
	s_waitcnt vmcnt(24)
	v_cvt_f32_fp8_e32 v180, v191
	v_cvt_f32_fp8_sdwa v181, v191 src0_sel:BYTE_1
	s_waitcnt lgkmcnt(0)
	v_lshl_add_u64 v[150:151], s[2:3], 0, v[150:151]
	v_lshl_add_u64 v[150:151], v[150:151], 0, v[74:75]
	v_pk_fma_f32 v[152:153], v[18:19], v[152:153], v[154:155] op_sel_hi:[0,1,1]
	v_pk_fma_f32 v[154:155], v[18:19], v[172:173], v[156:157] op_sel_hi:[0,1,1]
	v_pk_fma_f32 v[156:157], v[18:19], v[178:179], v[162:163] op_sel_hi:[0,1,1]
	v_pk_fma_f32 v[162:163], v[18:19], v[180:181], v[164:165] op_sel_hi:[0,1,1]
	v_lshl_add_u64 v[164:165], v[150:151], 0, s[8:9]
	v_add_co_u32_e64 v150, s[2:3], s72, v150
	s_mov_b32 s40, 35
	s_nop 0
	v_addc_co_u32_e64 v151, s[2:3], 0, v151, s[2:3]
	global_load_dword v215, v[150:151], off nt
	global_load_dword v216, v[164:165], off offset:256 nt
	global_load_dword v217, v[164:165], off offset:512 nt
	global_load_dword v218, v[164:165], off offset:768 nt
	s_ashr_i32 s41, s40, 31
	s_lshl_b64 s[2:3], s[40:41], 3
	s_add_u32 s2, s0, s2
	v_cvt_f32_fp8_e32 v60, v188
	v_cvt_f32_fp8_sdwa v61, v188 src0_sel:BYTE_1
	v_cvt_f32_fp8_sdwa v174, v189 src0_sel:BYTE_2
	v_cvt_f32_fp8_sdwa v175, v189 src0_sel:BYTE_3
	v_cvt_f32_fp8_e32 v176, v190
	v_cvt_f32_fp8_sdwa v177, v190 src0_sel:BYTE_1
	v_cvt_f32_fp8_sdwa v182, v191 src0_sel:BYTE_2
	v_cvt_f32_fp8_sdwa v183, v191 src0_sel:BYTE_3
	s_addc_u32 s3, s1, s3
	s_load_dwordx2 s[2:3], s[2:3], 0x0
	s_waitcnt vmcnt(27)
	v_cvt_f32_fp8_e32 v150, v192
	v_cvt_f32_fp8_sdwa v151, v192 src0_sel:BYTE_1
	v_pk_fma_f32 v[60:61], v[18:19], v[60:61], v[64:65] op_sel_hi:[0,1,1]
	v_pk_fma_f32 v[64:65], v[18:19], v[174:175], v[158:159] op_sel_hi:[0,1,1]
	v_pk_fma_f32 v[158:159], v[18:19], v[176:177], v[160:161] op_sel_hi:[0,1,1]
	v_pk_fma_f32 v[160:161], v[18:19], v[182:183], v[170:171] op_sel_hi:[0,1,1]
	v_cvt_f32_fp8_sdwa v164, v192 src0_sel:BYTE_2
	v_cvt_f32_fp8_sdwa v165, v192 src0_sel:BYTE_3
	s_waitcnt vmcnt(26)
	v_cvt_f32_fp8_e32 v170, v193
	v_cvt_f32_fp8_sdwa v171, v193 src0_sel:BYTE_1
	v_cvt_f32_fp8_sdwa v172, v193 src0_sel:BYTE_2
	v_cvt_f32_fp8_sdwa v173, v193 src0_sel:BYTE_3
	s_waitcnt vmcnt(25)
	v_cvt_f32_fp8_e32 v174, v194
	v_cvt_f32_fp8_sdwa v175, v194 src0_sel:BYTE_1
	v_cvt_f32_fp8_sdwa v176, v194 src0_sel:BYTE_2
	v_cvt_f32_fp8_sdwa v177, v194 src0_sel:BYTE_3
	s_waitcnt vmcnt(24)
	v_cvt_f32_fp8_e32 v178, v195
	v_cvt_f32_fp8_sdwa v179, v195 src0_sel:BYTE_1
	v_cvt_f32_fp8_sdwa v180, v195 src0_sel:BYTE_2
	v_cvt_f32_fp8_sdwa v181, v195 src0_sel:BYTE_3
	v_pk_fma_f32 v[150:151], v[18:19], v[150:151], v[60:61] op_sel:[1,0,0]
	s_waitcnt lgkmcnt(0)
	v_lshl_add_u64 v[60:61], s[2:3], 0, v[116:117]
	v_lshl_add_u64 v[60:61], v[60:61], 0, v[74:75]
	v_pk_fma_f32 v[152:153], v[18:19], v[164:165], v[152:153] op_sel:[1,0,0]
	v_pk_fma_f32 v[154:155], v[18:19], v[170:171], v[154:155] op_sel:[1,0,0]
	v_pk_fma_f32 v[164:165], v[18:19], v[172:173], v[64:65] op_sel:[1,0,0]
	v_pk_fma_f32 v[158:159], v[18:19], v[174:175], v[158:159] op_sel:[1,0,0]
	v_pk_fma_f32 v[156:157], v[18:19], v[176:177], v[156:157] op_sel:[1,0,0]
	v_pk_fma_f32 v[162:163], v[18:19], v[178:179], v[162:163] op_sel:[1,0,0]
	v_pk_fma_f32 v[160:161], v[18:19], v[180:181], v[160:161] op_sel:[1,0,0]
	v_mov_b64_e32 v[18:19], v[62:63]
	v_lshl_add_u64 v[62:63], v[60:61], 0, s[8:9]
	v_add_co_u32_e64 v60, s[2:3], s72, v60
	s_mov_b32 s30, 35
	s_nop 0
	v_addc_co_u32_e64 v61, s[2:3], 0, v61, s[2:3]
	global_load_dword v219, v[60:61], off nt
	global_load_dword v220, v[62:63], off offset:256 nt
	global_load_dword v221, v[62:63], off offset:512 nt
	global_load_dword v222, v[62:63], off offset:768 nt
	s_ashr_i32 s31, s30, 31
	s_lshl_b64 s[2:3], s[30:31], 3
	s_add_u32 s2, s0, s2
	s_addc_u32 s3, s1, s3
	s_load_dwordx2 s[2:3], s[2:3], 0x0
	s_mov_b32 s24, 35
	s_waitcnt vmcnt(27)
	v_cvt_f32_fp8_e32 v60, v196
	v_cvt_f32_fp8_sdwa v61, v196 src0_sel:BYTE_1
	v_cvt_f32_fp8_sdwa v62, v196 src0_sel:BYTE_2
	s_waitcnt lgkmcnt(0)
	v_lshl_add_u64 v[114:115], s[2:3], 0, v[114:115]
	v_lshl_add_u64 v[114:115], v[114:115], 0, v[74:75]
	v_lshl_add_u64 v[178:179], v[114:115], 0, s[8:9]
	v_add_co_u32_e64 v114, s[2:3], s72, v114
	v_cvt_f32_fp8_sdwa v63, v196 src0_sel:BYTE_3
	s_nop 0
	v_addc_co_u32_e64 v115, s[2:3], 0, v115, s[2:3]
	global_load_dword v223, v[114:115], off nt
	global_load_dword v224, v[178:179], off offset:256 nt
	global_load_dword v225, v[178:179], off offset:512 nt
	global_load_dword v226, v[178:179], off offset:768 nt
	s_ashr_i32 s25, s24, 31
	s_lshl_b64 s[2:3], s[24:25], 3
	s_add_u32 s2, s0, s2
	s_addc_u32 s3, s1, s3
	s_waitcnt vmcnt(30)
	v_cvt_f32_fp8_e32 v64, v197
	v_cvt_f32_fp8_sdwa v65, v197 src0_sel:BYTE_1
	v_cvt_f32_fp8_sdwa v116, v197 src0_sel:BYTE_2
	v_cvt_f32_fp8_sdwa v117, v197 src0_sel:BYTE_3
	s_waitcnt vmcnt(29)
	v_cvt_f32_fp8_e32 v170, v198
	v_cvt_f32_fp8_sdwa v171, v198 src0_sel:BYTE_1
	v_cvt_f32_fp8_sdwa v172, v198 src0_sel:BYTE_2
	v_cvt_f32_fp8_sdwa v173, v198 src0_sel:BYTE_3
	s_waitcnt vmcnt(28)
	v_cvt_f32_fp8_e32 v174, v199
	v_cvt_f32_fp8_sdwa v175, v199 src0_sel:BYTE_1
	v_cvt_f32_fp8_sdwa v176, v199 src0_sel:BYTE_2
	v_cvt_f32_fp8_sdwa v177, v199 src0_sel:BYTE_3
	s_load_dwordx2 s[2:3], s[2:3], 0x0
	s_waitcnt vmcnt(27)
	v_cvt_f32_fp8_e32 v114, v200
	v_cvt_f32_fp8_sdwa v115, v200 src0_sel:BYTE_1
	v_cvt_f32_fp8_sdwa v178, v200 src0_sel:BYTE_2
	v_cvt_f32_fp8_sdwa v179, v200 src0_sel:BYTE_3
	s_waitcnt vmcnt(26)
	v_cvt_f32_fp8_e32 v180, v201
	v_cvt_f32_fp8_sdwa v181, v201 src0_sel:BYTE_1
	v_cvt_f32_fp8_sdwa v182, v201 src0_sel:BYTE_2
	v_cvt_f32_fp8_sdwa v183, v201 src0_sel:BYTE_3
	s_waitcnt vmcnt(25)
	v_cvt_f32_fp8_e32 v184, v202
	v_cvt_f32_fp8_sdwa v185, v202 src0_sel:BYTE_1
	v_cvt_f32_fp8_sdwa v186, v202 src0_sel:BYTE_2
	v_cvt_f32_fp8_sdwa v187, v202 src0_sel:BYTE_3
	s_waitcnt vmcnt(24)
	v_cvt_f32_fp8_e32 v188, v203
	v_cvt_f32_fp8_sdwa v189, v203 src0_sel:BYTE_1
	v_cvt_f32_fp8_sdwa v190, v203 src0_sel:BYTE_2
	v_cvt_f32_fp8_sdwa v191, v203 src0_sel:BYTE_3
	v_pk_fma_f32 v[62:63], v[20:21], v[62:63], 0 op_sel_hi:[0,1,0]
	v_pk_fma_f32 v[60:61], v[20:21], v[60:61], 0 op_sel_hi:[0,1,0]
	v_pk_fma_f32 v[116:117], v[20:21], v[116:117], 0 op_sel_hi:[0,1,0]
	v_pk_fma_f32 v[64:65], v[20:21], v[64:65], 0 op_sel_hi:[0,1,0]
	v_pk_fma_f32 v[172:173], v[20:21], v[172:173], 0 op_sel_hi:[0,1,0]
	v_pk_fma_f32 v[170:171], v[20:21], v[170:171], 0 op_sel_hi:[0,1,0]
	v_pk_fma_f32 v[176:177], v[20:21], v[176:177], 0 op_sel_hi:[0,1,0]
	v_pk_fma_f32 v[174:175], v[20:21], v[174:175], 0 op_sel_hi:[0,1,0]
	v_pk_fma_f32 v[60:61], v[20:21], v[114:115], v[60:61] op_sel:[1,0,0]
	v_pk_fma_f32 v[62:63], v[20:21], v[178:179], v[62:63] op_sel:[1,0,0]
	v_pk_fma_f32 v[64:65], v[20:21], v[180:181], v[64:65] op_sel:[1,0,0]
	v_pk_fma_f32 v[114:115], v[20:21], v[182:183], v[116:117] op_sel:[1,0,0]
	v_pk_fma_f32 v[116:117], v[20:21], v[184:185], v[170:171] op_sel:[1,0,0]
	v_pk_fma_f32 v[170:171], v[20:21], v[186:187], v[172:173] op_sel:[1,0,0]
	v_pk_fma_f32 v[172:173], v[20:21], v[188:189], v[174:175] op_sel:[1,0,0]
	v_pk_fma_f32 v[174:175], v[20:21], v[190:191], v[176:177] op_sel:[1,0,0]
	v_mov_b64_e32 v[20:21], v[56:57]
	s_waitcnt lgkmcnt(0)
	v_lshl_add_u64 v[56:57], s[2:3], 0, v[70:71]
	v_lshl_add_u64 v[56:57], v[56:57], 0, v[74:75]
	v_lshl_add_u64 v[70:71], v[56:57], 0, s[8:9]
	v_add_co_u32_e64 v56, s[2:3], s72, v56
	s_mov_b32 s20, 35
	s_nop 0
	v_addc_co_u32_e64 v57, s[2:3], 0, v57, s[2:3]
	global_load_dword v200, v[56:57], off nt
	global_load_dword v201, v[70:71], off offset:256 nt
	global_load_dword v202, v[70:71], off offset:512 nt
	global_load_dword v203, v[70:71], off offset:768 nt
	s_ashr_i32 s21, s20, 31
	s_lshl_b64 s[2:3], s[20:21], 3
	s_add_u32 s2, s0, s2
	s_addc_u32 s3, s1, s3
	s_load_dwordx2 s[2:3], s[2:3], 0x0
	s_waitcnt vmcnt(27)
	v_cvt_f32_fp8_sdwa v70, v204 src0_sel:BYTE_2
	v_cvt_f32_fp8_sdwa v71, v204 src0_sel:BYTE_3
	s_waitcnt vmcnt(25)
	v_cvt_f32_fp8_sdwa v182, v206 src0_sel:BYTE_2
	v_cvt_f32_fp8_sdwa v183, v206 src0_sel:BYTE_3
	s_waitcnt vmcnt(24)
	v_cvt_f32_fp8_e32 v184, v207
	v_cvt_f32_fp8_sdwa v185, v207 src0_sel:BYTE_1
	s_waitcnt lgkmcnt(0)
	v_lshl_add_u64 v[68:69], s[2:3], 0, v[68:69]
	v_lshl_add_u64 v[68:69], v[68:69], 0, v[74:75]
	v_pk_fma_f32 v[62:63], v[22:23], v[70:71], v[62:63] op_sel_hi:[0,1,1]
	v_pk_fma_f32 v[70:71], v[22:23], v[182:183], v[170:171] op_sel_hi:[0,1,1]
	v_pk_fma_f32 v[170:171], v[22:23], v[184:185], v[172:173] op_sel_hi:[0,1,1]
	v_lshl_add_u64 v[172:173], v[68:69], 0, s[8:9]
	v_add_co_u32_e64 v68, s[2:3], s72, v68
	s_mov_b32 s16, 35
	s_nop 0
	v_addc_co_u32_e64 v69, s[2:3], 0, v69, s[2:3]
	v_cvt_f32_fp8_e32 v56, v204
	v_cvt_f32_fp8_sdwa v57, v204 src0_sel:BYTE_1
	v_cvt_f32_fp8_e32 v176, v205
	v_cvt_f32_fp8_sdwa v177, v205 src0_sel:BYTE_1
	v_cvt_f32_fp8_sdwa v178, v205 src0_sel:BYTE_2
	v_cvt_f32_fp8_sdwa v179, v205 src0_sel:BYTE_3
	v_cvt_f32_fp8_e32 v180, v206
	v_cvt_f32_fp8_sdwa v181, v206 src0_sel:BYTE_1
	v_cvt_f32_fp8_sdwa v186, v207 src0_sel:BYTE_2
	v_cvt_f32_fp8_sdwa v187, v207 src0_sel:BYTE_3
	global_load_dword v204, v[68:69], off nt
	global_load_dword v205, v[172:173], off offset:256 nt
	global_load_dword v206, v[172:173], off offset:512 nt
	global_load_dword v207, v[172:173], off offset:768 nt
	s_ashr_i32 s17, s16, 31
	s_lshl_b64 s[2:3], s[16:17], 3
	s_add_u32 s2, s0, s2
	s_addc_u32 s3, s1, s3
	s_load_dwordx2 s[2:3], s[2:3], 0x0
	s_waitcnt vmcnt(27)
	v_cvt_f32_fp8_e32 v68, v169
	v_cvt_f32_fp8_sdwa v69, v169 src0_sel:BYTE_1
	v_pk_fma_f32 v[56:57], v[22:23], v[56:57], v[60:61] op_sel_hi:[0,1,1]
	v_pk_fma_f32 v[60:61], v[22:23], v[178:179], v[114:115] op_sel_hi:[0,1,1]
	v_pk_fma_f32 v[64:65], v[22:23], v[176:177], v[64:65] op_sel_hi:[0,1,1]
	v_pk_fma_f32 v[114:115], v[22:23], v[180:181], v[116:117] op_sel_hi:[0,1,1]
	v_pk_fma_f32 v[116:117], v[22:23], v[186:187], v[174:175] op_sel_hi:[0,1,1]
	v_cvt_f32_fp8_sdwa v172, v169 src0_sel:BYTE_2
	v_cvt_f32_fp8_sdwa v173, v169 src0_sel:BYTE_3
	s_waitcnt vmcnt(26)
	v_cvt_f32_fp8_e32 v174, v208
	v_cvt_f32_fp8_sdwa v175, v208 src0_sel:BYTE_1
	v_cvt_f32_fp8_sdwa v176, v208 src0_sel:BYTE_2
	v_cvt_f32_fp8_sdwa v177, v208 src0_sel:BYTE_3
	s_waitcnt vmcnt(25)
	v_cvt_f32_fp8_e32 v178, v209
	v_cvt_f32_fp8_sdwa v179, v209 src0_sel:BYTE_1
	v_cvt_f32_fp8_sdwa v180, v209 src0_sel:BYTE_2
	v_cvt_f32_fp8_sdwa v181, v209 src0_sel:BYTE_3
	s_waitcnt vmcnt(24)
	v_cvt_f32_fp8_e32 v182, v210
	v_cvt_f32_fp8_sdwa v183, v210 src0_sel:BYTE_1
	v_cvt_f32_fp8_sdwa v184, v210 src0_sel:BYTE_2
	v_cvt_f32_fp8_sdwa v185, v210 src0_sel:BYTE_3
	v_pk_fma_f32 v[186:187], v[22:23], v[68:69], v[56:57] op_sel:[1,0,0]
	s_waitcnt lgkmcnt(0)
	v_lshl_add_u64 v[56:57], s[2:3], 0, v[66:67]
	v_lshl_add_u64 v[56:57], v[56:57], 0, v[74:75]
	v_pk_fma_f32 v[172:173], v[22:23], v[172:173], v[62:63] op_sel:[1,0,0]
	v_pk_fma_f32 v[174:175], v[22:23], v[174:175], v[64:65] op_sel:[1,0,0]
	v_pk_fma_f32 v[176:177], v[22:23], v[176:177], v[60:61] op_sel:[1,0,0]
	v_pk_fma_f32 v[178:179], v[22:23], v[178:179], v[114:115] op_sel:[1,0,0]
	v_pk_fma_f32 v[180:181], v[22:23], v[180:181], v[70:71] op_sel:[1,0,0]
	v_pk_fma_f32 v[170:171], v[22:23], v[182:183], v[170:171] op_sel:[1,0,0]
	v_pk_fma_f32 v[182:183], v[22:23], v[184:185], v[116:117] op_sel:[1,0,0]
	v_mov_b64_e32 v[22:23], v[58:59]
	v_lshl_add_u64 v[58:59], v[56:57], 0, s[8:9]
	v_add_co_u32_e64 v56, s[2:3], s72, v56
	s_mov_b32 s12, 35
	s_nop 0
	v_addc_co_u32_e64 v57, s[2:3], 0, v57, s[2:3]
	global_load_dword v208, v[56:57], off nt
	global_load_dword v209, v[58:59], off offset:256 nt
	global_load_dword v210, v[58:59], off offset:512 nt
	global_load_dword v227, v[58:59], off offset:768 nt
	ds_read_b128 v[68:71], v168
	ds_read_b128 v[64:67], v168 offset:1024
	ds_read_b128 v[60:63], v168 offset:2048
	ds_read_b128 v[56:59], v168 offset:3072
	s_ashr_i32 s13, s12, 31
	s_lshl_b64 s[2:3], s[12:13], 3
	s_waitcnt vmcnt(27)
	v_cvt_f32_fp8_e32 v168, v211
	v_cvt_f32_fp8_sdwa v169, v211 src0_sel:BYTE_1
	s_add_u32 s2, s0, s2
	s_waitcnt vmcnt(26)
	v_cvt_f32_fp8_e32 v188, v212
	v_cvt_f32_fp8_sdwa v189, v212 src0_sel:BYTE_1
	v_cvt_f32_fp8_sdwa v190, v212 src0_sel:BYTE_2
	v_cvt_f32_fp8_sdwa v191, v212 src0_sel:BYTE_3
	s_waitcnt vmcnt(25)
	v_cvt_f32_fp8_e32 v192, v213
	v_cvt_f32_fp8_sdwa v193, v213 src0_sel:BYTE_1
	s_addc_u32 s3, s1, s3
	s_load_dwordx2 s[2:3], s[2:3], 0x0
	v_cvt_f32_fp8_sdwa v194, v213 src0_sel:BYTE_2
	v_cvt_f32_fp8_sdwa v195, v213 src0_sel:BYTE_3
	s_waitcnt lgkmcnt(0)
	v_pk_fma_f32 v[152:153], v[70:71], v[152:153], v[122:123]
	v_pk_fma_f32 v[150:151], v[68:69], v[150:151], v[118:119]
	v_pk_fma_f32 v[164:165], v[66:67], v[164:165], v[126:127]
	v_pk_fma_f32 v[154:155], v[64:65], v[154:155], v[120:121]
	v_pk_fma_f32 v[130:131], v[62:63], v[156:157], v[130:131]
	v_pk_fma_f32 v[156:157], v[60:61], v[158:159], v[124:125]
	v_pk_fma_f32 v[158:159], v[56:57], v[162:163], v[128:129]
	v_pk_fma_f32 v[120:121], v[70:71], v[172:173], v[138:139]
	v_pk_fma_f32 v[128:129], v[68:69], v[186:187], v[132:133]
	v_pk_fma_f32 v[114:115], v[66:67], v[176:177], v[142:143]
	v_pk_fma_f32 v[122:123], v[64:65], v[174:175], v[136:137]
	v_pk_fma_f32 v[134:135], v[58:59], v[160:161], v[134:135]
	v_pk_fma_f32 v[116:117], v[62:63], v[180:181], v[146:147]
	v_pk_fma_f32 v[124:125], v[60:61], v[178:179], v[140:141]
	v_pk_fma_f32 v[118:119], v[58:59], v[182:183], v[148:149]
	v_pk_fma_f32 v[126:127], v[56:57], v[170:171], v[144:145]
	v_pk_fma_f32 v[136:137], v[24:25], v[168:169], 0 op_sel_hi:[0,1,0]
	v_pk_mul_f32 v[160:161], v[150:151], v[150:151]
	v_pk_mul_f32 v[162:163], v[152:153], v[152:153]
	v_pk_mul_f32 v[168:169], v[154:155], v[154:155]
	v_pk_mul_f32 v[170:171], v[164:165], v[164:165]
	v_mul_f32_e32 v172, v157, v157
	v_mul_f32_e32 v174, v131, v131
	v_pk_mul_f32 v[176:177], v[128:129], v[128:129]
	v_pk_mul_f32 v[178:179], v[120:121], v[120:121]
	v_pk_mul_f32 v[180:181], v[122:123], v[122:123]
	v_pk_mul_f32 v[182:183], v[114:115], v[114:115]
	v_pk_fma_f32 v[138:139], v[24:25], v[190:191], 0 op_sel_hi:[0,1,0]
	v_pk_fma_f32 v[140:141], v[24:25], v[188:189], 0 op_sel_hi:[0,1,0]
	v_pk_fma_f32 v[144:145], v[24:25], v[192:193], 0 op_sel_hi:[0,1,0]
	v_mul_f32_e32 v191, v134, v134
	v_mul_f32_e32 v192, v135, v135
	v_pk_mov_b32 v[188:189], v[160:161], v[162:163] op_sel:[1,0]
	v_mov_b32_e32 v161, v163
	v_pk_mov_b32 v[162:163], v[168:169], v[170:171] op_sel:[1,0]
	v_mov_b32_e32 v169, v171
	v_pk_fma_f32 v[170:171], v[156:157], v[156:157], v[172:173] op_sel_hi:[1,1,0]
	v_pk_fma_f32 v[172:173], v[130:131], v[130:131], v[174:175] op_sel_hi:[1,1,0]
	v_pk_mov_b32 v[174:175], v[176:177], v[178:179] op_sel:[1,0]
	v_mov_b32_e32 v177, v179
	v_pk_mov_b32 v[178:179], v[180:181], v[182:183] op_sel:[1,0]
	v_mov_b32_e32 v181, v183
	v_pk_add_f32 v[160:161], v[188:189], v[160:161]
	v_pk_add_f32 v[162:163], v[162:163], v[168:169]
	v_mov_b32_e32 v171, v191
	v_mov_b32_e32 v173, v192
	v_pk_add_f32 v[168:169], v[174:175], v[176:177]
	v_pk_add_f32 v[174:175], v[178:179], v[180:181]
	v_pk_fma_f32 v[142:143], v[24:25], v[194:195], 0 op_sel_hi:[0,1,0]
	v_mul_f32_e32 v187, v158, v158
	v_mul_f32_e32 v190, v159, v159
	v_mul_f32_e32 v193, v126, v126
	v_mul_f32_e32 v194, v127, v127
	v_pk_add_f32 v[160:161], v[160:161], v[160:161] op_sel:[0,1] op_sel_hi:[1,0]
	v_pk_add_f32 v[162:163], v[162:163], v[162:163] op_sel:[0,1] op_sel_hi:[1,0]
	v_pk_add_f32 v[170:171], v[170:171], v[172:173]
	v_pk_add_f32 v[168:169], v[168:169], v[168:169] op_sel:[0,1] op_sel_hi:[1,0]
	v_pk_add_f32 v[172:173], v[174:175], v[174:175] op_sel:[0,1] op_sel_hi:[1,0]
	v_lshl_add_u64 v[96:97], s[2:3], 0, v[96:97]
	v_mov_b32_e32 v161, v187
	v_mov_b32_e32 v163, v190
	v_mov_b32_e32 v169, v193
	v_mov_b32_e32 v173, v194
	v_lshl_add_u64 v[96:97], v[96:97], 0, v[74:75]
	v_pk_add_f32 v[160:161], v[160:161], v[162:163]
	v_pk_add_f32 v[162:163], v[168:169], v[172:173]
	v_lshl_add_u64 v[168:169], v[96:97], 0, s[8:9]
	v_add_co_u32_e64 v96, s[2:3], s72, v96
	v_cvt_f32_fp8_sdwa v184, v211 src0_sel:BYTE_2
	s_nop 0
	v_addc_co_u32_e64 v97, s[2:3], 0, v97, s[2:3]
	global_load_dword v178, v[96:97], off nt
	global_load_dword v179, v[168:169], off offset:256 nt
	global_load_dword v180, v[168:169], off offset:512 nt
	global_load_dword v181, v[168:169], off offset:768 nt
	v_cvt_f32_fp8_sdwa v185, v211 src0_sel:BYTE_3
	s_waitcnt vmcnt(28)
	v_cvt_f32_fp8_e32 v196, v214
	v_cvt_f32_fp8_sdwa v197, v214 src0_sel:BYTE_1
	v_pk_add_f32 v[160:161], v[160:161], v[170:171]
	v_pk_fma_f32 v[132:133], v[24:25], v[184:185], 0 op_sel_hi:[0,1,0]
	v_mul_f32_e32 v184, v125, v125
	v_mul_f32_e32 v186, v117, v117
	v_add_f32_e32 v74, v160, v161
	v_pk_fma_f32 v[148:149], v[24:25], v[196:197], 0 op_sel_hi:[0,1,0]
	v_mul_f32_e32 v195, v118, v118
	v_mul_f32_e32 v196, v119, v119
	v_pk_fma_f32 v[182:183], v[124:125], v[124:125], v[184:185] op_sel_hi:[1,1,0]
	v_pk_fma_f32 v[184:185], v[116:117], v[116:117], v[186:187] op_sel_hi:[1,1,0]
	v_add_f32_dpp v74, v74, v74 quad_perm:[1,0,3,2] row_mask:0xf bank_mask:0xf bound_ctrl:1
	v_mov_b32_e32 v183, v195
	v_mov_b32_e32 v185, v196
	v_add_f32_dpp v74, v74, v74 quad_perm:[2,3,0,1] row_mask:0xf bank_mask:0xf bound_ctrl:1
	v_pk_add_f32 v[174:175], v[182:183], v[184:185]
	v_mbcnt_lo_u32_b32 v96, -1, 0
	v_mbcnt_hi_u32_b32 v96, -1, v96
	v_cvt_f32_fp8_sdwa v198, v214 src0_sel:BYTE_2
	v_lshlrev_b32_e32 v182, 2, v96
	v_add_f32_dpp v74, v74, v74 row_half_mirror row_mask:0xf bank_mask:0xf bound_ctrl:1
	v_pk_add_f32 v[162:163], v[162:163], v[174:175]
	v_xor_b32_e32 v182, 64, v182
	v_add_f32_dpp v74, v74, v74 row_mirror row_mask:0xf bank_mask:0xf bound_ctrl:1
	v_cvt_f32_fp8_sdwa v199, v214 src0_sel:BYTE_3
	v_add_f32_e32 v97, v162, v163
	ds_bpermute_b32 v182, v182, v74
	s_waitcnt vmcnt(27)
	v_cvt_f32_fp8_e32 v96, v215
	v_add_f32_dpp v183, v97, v97 quad_perm:[1,0,3,2] row_mask:0xf bank_mask:0xf bound_ctrl:1
	v_cvt_f32_fp8_sdwa v97, v215 src0_sel:BYTE_1
	v_cvt_f32_fp8_sdwa v160, v215 src0_sel:BYTE_2
	v_cvt_f32_fp8_sdwa v161, v215 src0_sel:BYTE_3
	s_waitcnt vmcnt(26)
	v_cvt_f32_fp8_e32 v162, v216
	v_cvt_f32_fp8_sdwa v163, v216 src0_sel:BYTE_1
	v_cvt_f32_fp8_sdwa v168, v216 src0_sel:BYTE_2
	v_cvt_f32_fp8_sdwa v169, v216 src0_sel:BYTE_3
	s_waitcnt vmcnt(25)
	v_cvt_f32_fp8_e32 v170, v217
	v_cvt_f32_fp8_sdwa v171, v217 src0_sel:BYTE_1
	v_cvt_f32_fp8_sdwa v172, v217 src0_sel:BYTE_2
	v_cvt_f32_fp8_sdwa v173, v217 src0_sel:BYTE_3
	s_waitcnt vmcnt(24)
	v_cvt_f32_fp8_e32 v174, v218
	v_cvt_f32_fp8_sdwa v175, v218 src0_sel:BYTE_1
	v_cvt_f32_fp8_sdwa v176, v218 src0_sel:BYTE_2
	v_cvt_f32_fp8_sdwa v177, v218 src0_sel:BYTE_3
	v_pk_fma_f32 v[146:147], v[24:25], v[198:199], 0 op_sel_hi:[0,1,0]
	v_pk_fma_f32 v[96:97], v[24:25], v[96:97], v[136:137] op_sel:[1,0,0]
	v_pk_fma_f32 v[132:133], v[24:25], v[160:161], v[132:133] op_sel:[1,0,0]
	v_pk_fma_f32 v[136:137], v[24:25], v[162:163], v[140:141] op_sel:[1,0,0]
	v_pk_fma_f32 v[138:139], v[24:25], v[168:169], v[138:139] op_sel:[1,0,0]
	v_pk_fma_f32 v[140:141], v[24:25], v[170:171], v[144:145] op_sel:[1,0,0]
	v_pk_fma_f32 v[142:143], v[24:25], v[172:173], v[142:143] op_sel:[1,0,0]
	v_pk_fma_f32 v[144:145], v[24:25], v[174:175], v[148:149] op_sel:[1,0,0]
	v_pk_fma_f32 v[146:147], v[24:25], v[176:177], v[146:147] op_sel:[1,0,0]
	v_mov_b64_e32 v[24:25], v[52:53]
	s_waitcnt lgkmcnt(0)
	v_add_f32_e32 v52, v74, v182
	v_mov_b32_e32 v53, v52
	s_mov_b32 s66, 34
	s_nop 1
	v_permlane32_swap_b32 v52, v53
	s_ashr_i32 s67, s66, 31
	v_add_f32_e32 v52, v52, v53
	v_fmamk_f32 v74, v52, 0x3a800000, v73
	s_lshl_b64 s[10:11], s[66:67], 3
	v_mul_f32_e32 v176, 0x4b800000, v74
	s_add_u32 s10, s0, s10
	v_cmp_gt_f32_e64 s[2:3], s74, v74
	s_addc_u32 s11, s1, s11
	s_waitcnt vmcnt(23)
	v_cvt_f32_fp8_sdwa v148, v219 src0_sel:BYTE_2
	v_cndmask_b32_e64 v74, v74, v176, s[2:3]
	v_cvt_f32_fp8_sdwa v149, v219 src0_sel:BYTE_3
	v_rsq_f32_e32 v74, v74
	s_load_dwordx2 s[10:11], s[10:11], 0x0
	v_cvt_f32_fp8_e32 v52, v219
	v_cvt_f32_fp8_sdwa v53, v219 src0_sel:BYTE_1
	s_waitcnt vmcnt(22)
	v_cvt_f32_fp8_e32 v160, v220
	v_cvt_f32_fp8_sdwa v161, v220 src0_sel:BYTE_1
	v_cvt_f32_fp8_sdwa v162, v220 src0_sel:BYTE_2
	v_cvt_f32_fp8_sdwa v163, v220 src0_sel:BYTE_3
	s_waitcnt vmcnt(21)
	v_cvt_f32_fp8_e32 v168, v221
	v_cvt_f32_fp8_sdwa v169, v221 src0_sel:BYTE_1
	v_cvt_f32_fp8_sdwa v170, v221 src0_sel:BYTE_2
	v_cvt_f32_fp8_sdwa v171, v221 src0_sel:BYTE_3
	s_waitcnt vmcnt(20)
	v_cvt_f32_fp8_e32 v172, v222
	v_cvt_f32_fp8_sdwa v173, v222 src0_sel:BYTE_1
	v_pk_fma_f32 v[148:149], v[26:27], v[148:149], v[132:133] op_sel_hi:[0,1,1]
	v_mul_f32_e32 v132, 0x45800000, v74
	v_cndmask_b32_e64 v74, v74, v132, s[2:3]
	s_waitcnt lgkmcnt(0)
	v_lshl_add_u64 v[132:133], s[10:11], 0, v[78:79]
	v_pk_fma_f32 v[52:53], v[26:27], v[52:53], v[96:97] op_sel_hi:[0,1,1]
	v_pk_fma_f32 v[96:97], v[26:27], v[162:163], v[138:139] op_sel_hi:[0,1,1]
	v_pk_fma_f32 v[160:161], v[26:27], v[160:161], v[136:137] op_sel_hi:[0,1,1]
	v_pk_mul_f32 v[136:137], v[150:151], v[74:75] op_sel_hi:[1,0]
	v_pk_mul_f32 v[138:139], v[152:153], v[74:75] op_sel_hi:[1,0]
	v_add_co_u32_e64 v150, s[2:3], s75, v132
	v_pk_fma_f32 v[162:163], v[26:27], v[170:171], v[142:143] op_sel_hi:[0,1,1]
	v_pk_fma_f32 v[168:169], v[26:27], v[168:169], v[140:141] op_sel_hi:[0,1,1]
	v_pk_fma_f32 v[170:171], v[26:27], v[172:173], v[144:145] op_sel_hi:[0,1,1]
	v_addc_co_u32_e64 v151, s[2:3], -1, v133, s[2:3]
	v_pk_mul_f32 v[140:141], v[154:155], v[74:75] op_sel_hi:[1,0]
	v_pk_mul_f32 v[142:143], v[164:165], v[74:75] op_sel_hi:[1,0]
	v_pk_mul_f32 v[144:145], v[156:157], v[74:75] op_sel_hi:[1,0]
	v_pk_mul_f32 v[152:153], v[130:131], v[74:75] op_sel_hi:[1,0]
	v_pk_mul_f32 v[154:155], v[158:159], v[74:75] op_sel_hi:[1,0]
	v_pk_mul_f32 v[156:157], v[134:135], v[74:75] op_sel_hi:[1,0]
	v_pk_mul_f32 v[132:133], v[2:3], v[138:139]
	v_pk_mul_f32 v[130:131], v[0:1], v[136:137]
	v_add_f32_dpp v183, v183, v183 quad_perm:[2,3,0,1] row_mask:0xf bank_mask:0xf bound_ctrl:1
	v_pk_mul_f32 v[136:137], v[6:7], v[142:143]
	v_pk_mul_f32 v[134:135], v[4:5], v[140:141]
	v_pk_mul_f32 v[140:141], v[10:11], v[152:153]
	v_pk_mul_f32 v[138:139], v[8:9], v[144:145]
	v_pk_mul_f32 v[144:145], v[14:15], v[156:157]
	v_pk_mul_f32 v[142:143], v[12:13], v[154:155]
	global_store_dwordx4 v[150:151], v[130:133], off offset:-3072
	global_store_dwordx4 v[150:151], v[134:137], off offset:-2048
	global_store_dwordx4 v[150:151], v[138:141], off offset:-1024
	global_store_dwordx4 v[150:151], v[142:145], off
	v_mbcnt_lo_u32_b32 v74, -1, 0
	v_mbcnt_hi_u32_b32 v74, -1, v74
	v_add_f32_dpp v183, v183, v183 row_half_mirror row_mask:0xf bank_mask:0xf bound_ctrl:1
	v_lshlrev_b32_e32 v74, 2, v74
	v_xor_b32_e32 v74, 64, v74
	v_add_f32_dpp v183, v183, v183 row_mirror row_mask:0xf bank_mask:0xf bound_ctrl:1
	v_cvt_f32_fp8_sdwa v174, v222 src0_sel:BYTE_2
	v_cvt_f32_fp8_sdwa v175, v222 src0_sel:BYTE_3
	s_waitcnt vmcnt(23)
	v_cvt_f32_fp8_e32 v130, v223
	v_cvt_f32_fp8_sdwa v131, v223 src0_sel:BYTE_1
	v_cvt_f32_fp8_sdwa v132, v223 src0_sel:BYTE_2
	v_cvt_f32_fp8_sdwa v133, v223 src0_sel:BYTE_3
	s_waitcnt vmcnt(22)
	v_cvt_f32_fp8_e32 v134, v224
	v_cvt_f32_fp8_sdwa v135, v224 src0_sel:BYTE_1
	v_cvt_f32_fp8_sdwa v136, v224 src0_sel:BYTE_2
	v_cvt_f32_fp8_sdwa v137, v224 src0_sel:BYTE_3
	s_waitcnt vmcnt(21)
	v_cvt_f32_fp8_e32 v138, v225
	v_cvt_f32_fp8_sdwa v139, v225 src0_sel:BYTE_1
	v_cvt_f32_fp8_sdwa v140, v225 src0_sel:BYTE_2
	v_cvt_f32_fp8_sdwa v141, v225 src0_sel:BYTE_3
	ds_bpermute_b32 v74, v74, v183
	s_waitcnt vmcnt(20)
	v_cvt_f32_fp8_e32 v142, v226
	v_cvt_f32_fp8_sdwa v143, v226 src0_sel:BYTE_1
	v_cvt_f32_fp8_sdwa v144, v226 src0_sel:BYTE_2
	v_cvt_f32_fp8_sdwa v145, v226 src0_sel:BYTE_3
	v_lshlrev_b32_e32 v98, 16, v100
	v_and_b32_e32 v99, 0xffff0000, v100
	v_lshlrev_b32_e32 v102, 16, v101
	v_and_b32_e32 v103, 0xffff0000, v101
	v_lshlrev_b32_e32 v100, 16, v104
	v_and_b32_e32 v101, 0xffff0000, v104
	v_lshlrev_b32_e32 v106, 16, v105
	v_and_b32_e32 v107, 0xffff0000, v105
	v_lshlrev_b32_e32 v104, 16, v108
	v_and_b32_e32 v105, 0xffff0000, v108
	v_lshlrev_b32_e32 v110, 16, v109
	v_and_b32_e32 v111, 0xffff0000, v109
	v_pk_fma_f32 v[146:147], v[26:27], v[174:175], v[146:147] op_sel_hi:[0,1,1]
	v_pk_fma_f32 v[52:53], v[26:27], v[130:131], v[52:53] op_sel:[1,0,0]
	v_pk_fma_f32 v[130:131], v[26:27], v[132:133], v[148:149] op_sel:[1,0,0]
	v_pk_fma_f32 v[132:133], v[26:27], v[134:135], v[160:161] op_sel:[1,0,0]
	v_pk_fma_f32 v[96:97], v[26:27], v[136:137], v[96:97] op_sel:[1,0,0]
	v_pk_fma_f32 v[134:135], v[26:27], v[138:139], v[168:169] op_sel:[1,0,0]
	v_pk_fma_f32 v[136:137], v[26:27], v[140:141], v[162:163] op_sel:[1,0,0]
	v_lshlrev_b32_e32 v108, 16, v112
	v_and_b32_e32 v109, 0xffff0000, v112
	v_lshlrev_b32_e32 v112, 16, v113
	v_and_b32_e32 v113, 0xffff0000, v113
	v_pk_fma_f32 v[138:139], v[26:27], v[142:143], v[170:171] op_sel:[1,0,0]
	v_pk_fma_f32 v[140:141], v[26:27], v[144:145], v[146:147] op_sel:[1,0,0]
	v_pk_fma_f32 v[130:131], v[70:71], v[130:131], v[102:103]
	v_pk_fma_f32 v[142:143], v[68:69], v[52:53], v[98:99]
	v_pk_fma_f32 v[144:145], v[66:67], v[96:97], v[106:107]
	v_pk_fma_f32 v[132:133], v[64:65], v[132:133], v[100:101]
	v_pk_fma_f32 v[110:111], v[62:63], v[136:137], v[110:111]
	v_pk_fma_f32 v[134:135], v[60:61], v[134:135], v[104:105]
	s_waitcnt lgkmcnt(0)
	v_add_f32_e32 v104, v183, v74
	s_mov_b32 s64, 34
	v_mov_b64_e32 v[26:27], v[54:55]
	v_pk_fma_f32 v[112:113], v[58:59], v[140:141], v[112:113]
	v_mov_b32_e32 v105, v104
	v_pk_mul_f32 v[52:53], v[142:143], v[142:143]
	v_pk_mul_f32 v[54:55], v[130:131], v[130:131]
	v_pk_mul_f32 v[96:97], v[132:133], v[132:133]
	v_pk_mul_f32 v[98:99], v[144:145], v[144:145]
	v_mul_f32_e32 v74, v135, v135
	v_mul_f32_e32 v100, v111, v111
	v_mul_f32_e32 v136, v112, v112
	v_mul_f32_e32 v137, v113, v113
	s_nop 1
	v_permlane32_swap_b32 v104, v105
	v_pk_mov_b32 v[102:103], v[52:53], v[54:55] op_sel:[1,0]
	v_mov_b32_e32 v53, v55
	v_pk_mov_b32 v[54:55], v[96:97], v[98:99] op_sel:[1,0]
	v_mov_b32_e32 v97, v99
	v_pk_fma_f32 v[98:99], v[134:135], v[134:135], v[74:75] op_sel_hi:[1,1,0]
	v_pk_fma_f32 v[100:101], v[110:111], v[110:111], v[100:101] op_sel_hi:[1,1,0]
	v_add_f32_e32 v74, v104, v105
	s_ashr_i32 s65, s64, 31
	v_pk_fma_f32 v[108:109], v[56:57], v[138:139], v[108:109]
	v_pk_add_f32 v[52:53], v[102:103], v[52:53]
	v_pk_add_f32 v[54:55], v[54:55], v[96:97]
	v_mov_b32_e32 v99, v136
	v_mov_b32_e32 v101, v137
	v_fmamk_f32 v74, v74, 0x3a800000, v73
	s_lshl_b64 s[10:11], s[64:65], 3
	v_mul_f32_e32 v106, v108, v108
	v_mul_f32_e32 v107, v109, v109
	v_pk_add_f32 v[52:53], v[52:53], v[52:53] op_sel:[0,1] op_sel_hi:[1,0]
	v_pk_add_f32 v[54:55], v[54:55], v[54:55] op_sel:[0,1] op_sel_hi:[1,0]
	v_pk_add_f32 v[96:97], v[98:99], v[100:101]
	v_mul_f32_e32 v98, 0x4b800000, v74
	s_add_u32 s10, s0, s10
	v_cmp_gt_f32_e64 s[2:3], s74, v74
	v_mov_b32_e32 v53, v106
	v_mov_b32_e32 v55, v107
	v_cndmask_b32_e64 v74, v74, v98, s[2:3]
	s_addc_u32 s11, s1, s11
	v_pk_add_f32 v[52:53], v[52:53], v[54:55]
	v_rsq_f32_e32 v74, v74
	s_load_dwordx2 s[10:11], s[10:11], 0x0
	v_pk_add_f32 v[52:53], v[52:53], v[96:97]
	s_waitcnt vmcnt(19)
	v_cvt_f32_fp8_e32 v54, v200
	v_cvt_f32_fp8_sdwa v55, v200 src0_sel:BYTE_1
	v_cvt_f32_fp8_sdwa v96, v200 src0_sel:BYTE_2
	v_cvt_f32_fp8_sdwa v97, v200 src0_sel:BYTE_3
	s_waitcnt vmcnt(18)
	v_cvt_f32_fp8_e32 v98, v201
	v_cvt_f32_fp8_sdwa v99, v201 src0_sel:BYTE_1
	v_add_f32_e32 v52, v52, v53
	v_cvt_f32_fp8_sdwa v100, v201 src0_sel:BYTE_2
	v_cvt_f32_fp8_sdwa v101, v201 src0_sel:BYTE_3
	s_waitcnt vmcnt(17)
	v_cvt_f32_fp8_e32 v102, v202
	v_cvt_f32_fp8_sdwa v103, v202 src0_sel:BYTE_1
	v_cvt_f32_fp8_sdwa v104, v202 src0_sel:BYTE_2
	v_cvt_f32_fp8_sdwa v105, v202 src0_sel:BYTE_3
	s_waitcnt vmcnt(16)
	v_cvt_f32_fp8_e32 v106, v203
	v_cvt_f32_fp8_sdwa v107, v203 src0_sel:BYTE_1
	v_add_f32_dpp v52, v52, v52 quad_perm:[1,0,3,2] row_mask:0xf bank_mask:0xf bound_ctrl:1
	v_mul_f32_e32 v53, 0x45800000, v74
	v_pk_fma_f32 v[138:139], v[28:29], v[54:55], 0 op_sel_hi:[0,1,0]
	v_add_f32_dpp v52, v52, v52 quad_perm:[2,3,0,1] row_mask:0xf bank_mask:0xf bound_ctrl:1
	s_waitcnt lgkmcnt(0)
	v_lshl_add_u64 v[54:55], s[10:11], 0, v[78:79]
	v_pk_fma_f32 v[140:141], v[28:29], v[96:97], 0 op_sel_hi:[0,1,0]
	v_add_f32_dpp v156, v52, v52 row_half_mirror row_mask:0xf bank_mask:0xf bound_ctrl:1
	v_cndmask_b32_e64 v52, v74, v53, s[2:3]
	v_pk_fma_f32 v[146:147], v[28:29], v[98:99], 0 op_sel_hi:[0,1,0]
	v_pk_mul_f32 v[96:97], v[128:129], v[52:53] op_sel_hi:[1,0]
	v_pk_mul_f32 v[98:99], v[120:121], v[52:53] op_sel_hi:[1,0]
	v_add_co_u32_e64 v120, s[2:3], s76, v54
	v_pk_fma_f32 v[148:149], v[28:29], v[100:101], 0 op_sel_hi:[0,1,0]
	v_pk_fma_f32 v[150:151], v[28:29], v[104:105], 0 op_sel_hi:[0,1,0]
	v_pk_fma_f32 v[152:153], v[28:29], v[102:103], 0 op_sel_hi:[0,1,0]
	v_pk_fma_f32 v[154:155], v[28:29], v[106:107], 0 op_sel_hi:[0,1,0]
	v_addc_co_u32_e64 v121, s[2:3], -1, v55, s[2:3]
	v_pk_mul_f32 v[100:101], v[122:123], v[52:53] op_sel_hi:[1,0]
	v_pk_mul_f32 v[102:103], v[114:115], v[52:53] op_sel_hi:[1,0]
	v_pk_mul_f32 v[104:105], v[124:125], v[52:53] op_sel_hi:[1,0]
	v_pk_mul_f32 v[106:107], v[116:117], v[52:53] op_sel_hi:[1,0]
	v_pk_mul_f32 v[114:115], v[126:127], v[52:53] op_sel_hi:[1,0]
	v_pk_mul_f32 v[116:117], v[118:119], v[52:53] op_sel_hi:[1,0]
	v_pk_mul_f32 v[54:55], v[2:3], v[98:99]
	v_pk_mul_f32 v[52:53], v[0:1], v[96:97]
	v_pk_mul_f32 v[98:99], v[6:7], v[102:103]
	v_pk_mul_f32 v[96:97], v[4:5], v[100:101]
	v_pk_mul_f32 v[102:103], v[10:11], v[106:107]
	v_pk_mul_f32 v[100:101], v[8:9], v[104:105]
	v_pk_mul_f32 v[106:107], v[14:15], v[116:117]
	v_pk_mul_f32 v[104:105], v[12:13], v[114:115]
	global_store_dwordx4 v[120:121], v[52:55], off offset:-3072
	global_store_dwordx4 v[120:121], v[96:99], off offset:-2048
	global_store_dwordx4 v[120:121], v[100:103], off offset:-1024
	global_store_dwordx4 v[120:121], v[104:107], off
	v_mbcnt_lo_u32_b32 v52, -1, 0
	v_mbcnt_hi_u32_b32 v52, -1, v52
	v_add_f32_dpp v74, v156, v156 row_mirror row_mask:0xf bank_mask:0xf bound_ctrl:1
	v_lshlrev_b32_e32 v52, 2, v52
	v_xor_b32_e32 v52, 64, v52
	ds_bpermute_b32 v114, v52, v74
	v_cvt_f32_fp8_sdwa v136, v203 src0_sel:BYTE_2
	v_cvt_f32_fp8_sdwa v137, v203 src0_sel:BYTE_3
	s_waitcnt vmcnt(19)
	v_cvt_f32_fp8_e32 v52, v204
	v_cvt_f32_fp8_sdwa v53, v204 src0_sel:BYTE_1
	v_cvt_f32_fp8_sdwa v54, v204 src0_sel:BYTE_2
	v_cvt_f32_fp8_sdwa v55, v204 src0_sel:BYTE_3
	s_waitcnt vmcnt(18)
	v_cvt_f32_fp8_e32 v96, v205
	v_cvt_f32_fp8_sdwa v97, v205 src0_sel:BYTE_1
	v_cvt_f32_fp8_sdwa v98, v205 src0_sel:BYTE_2
	v_cvt_f32_fp8_sdwa v99, v205 src0_sel:BYTE_3
	s_waitcnt vmcnt(17)
	v_cvt_f32_fp8_e32 v100, v206
	v_cvt_f32_fp8_sdwa v101, v206 src0_sel:BYTE_1
	v_cvt_f32_fp8_sdwa v102, v206 src0_sel:BYTE_2
	v_cvt_f32_fp8_sdwa v103, v206 src0_sel:BYTE_3
	s_waitcnt vmcnt(16)
	v_cvt_f32_fp8_e32 v104, v207
	v_cvt_f32_fp8_sdwa v105, v207 src0_sel:BYTE_1
	v_cvt_f32_fp8_sdwa v106, v207 src0_sel:BYTE_2
	v_cvt_f32_fp8_sdwa v107, v207 src0_sel:BYTE_3
	s_waitcnt lgkmcnt(0)
	v_add_f32_e32 v74, v74, v114
	s_mov_b32 s68, 34
	v_pk_fma_f32 v[136:137], v[28:29], v[136:137], 0 op_sel_hi:[0,1,0]
	v_mov_b32_e32 v156, v74
	v_pk_fma_f32 v[114:115], v[28:29], v[54:55], v[140:141] op_sel:[1,0,0]
	v_pk_fma_f32 v[116:117], v[28:29], v[52:53], v[138:139] op_sel:[1,0,0]
	v_pk_fma_f32 v[118:119], v[28:29], v[98:99], v[148:149] op_sel:[1,0,0]
	v_pk_fma_f32 v[120:121], v[28:29], v[96:97], v[146:147] op_sel:[1,0,0]
	v_pk_fma_f32 v[122:123], v[28:29], v[100:101], v[152:153] op_sel:[1,0,0]
	v_pk_fma_f32 v[124:125], v[28:29], v[102:103], v[150:151] op_sel:[1,0,0]
	v_pk_fma_f32 v[126:127], v[28:29], v[104:105], v[154:155] op_sel:[1,0,0]
	v_pk_fma_f32 v[128:129], v[28:29], v[106:107], v[136:137] op_sel:[1,0,0]
	s_nop 1
	v_permlane32_swap_b32 v74, v156
	v_mov_b64_e32 v[28:29], v[48:49]
	v_add_f32_e32 v48, v74, v156
	s_ashr_i32 s69, s68, 31
	v_fmamk_f32 v48, v48, 0x3a800000, v73
	s_lshl_b64 s[10:11], s[68:69], 3
	v_mul_f32_e32 v49, 0x4b800000, v48
	s_add_u32 s10, s0, s10
	v_cmp_gt_f32_e64 s[2:3], s74, v48
	s_addc_u32 s11, s1, s11
	s_load_dwordx2 s[10:11], s[10:11], 0x0
	v_cndmask_b32_e64 v48, v48, v49, s[2:3]
	v_rsq_f32_e32 v52, v48
	s_waitcnt vmcnt(15)
	v_cvt_f32_fp8_e32 v48, v208
	v_cvt_f32_fp8_sdwa v49, v208 src0_sel:BYTE_1
	s_waitcnt lgkmcnt(0)
	v_lshl_add_u64 v[154:155], s[10:11], 0, v[78:79]
	v_mul_f32_e32 v53, 0x45800000, v52
	v_cndmask_b32_e64 v52, v52, v53, s[2:3]
	s_waitcnt vmcnt(13)
	v_cvt_f32_fp8_e32 v146, v210
	v_cvt_f32_fp8_sdwa v147, v210 src0_sel:BYTE_1
	v_pk_mul_f32 v[96:97], v[142:143], v[52:53] op_sel_hi:[1,0]
	v_pk_mul_f32 v[54:55], v[130:131], v[52:53] op_sel_hi:[1,0]
	v_add_co_u32_e64 v130, s[2:3], s73, v154
	v_pk_mul_f32 v[100:101], v[132:133], v[52:53] op_sel_hi:[1,0]
	s_nop 0
	v_addc_co_u32_e64 v131, s[2:3], -1, v155, s[2:3]
	v_pk_mul_f32 v[98:99], v[144:145], v[52:53] op_sel_hi:[1,0]
	v_pk_mul_f32 v[104:105], v[134:135], v[52:53] op_sel_hi:[1,0]
	v_pk_mul_f32 v[102:103], v[110:111], v[52:53] op_sel_hi:[1,0]
	v_pk_mul_f32 v[108:109], v[108:109], v[52:53] op_sel_hi:[1,0]
	v_pk_mul_f32 v[106:107], v[112:113], v[52:53] op_sel_hi:[1,0]
	v_pk_mul_f32 v[54:55], v[2:3], v[54:55]
	v_pk_mul_f32 v[52:53], v[0:1], v[96:97]
	v_pk_mul_f32 v[98:99], v[6:7], v[98:99]
	v_pk_mul_f32 v[96:97], v[4:5], v[100:101]
	v_pk_mul_f32 v[102:103], v[10:11], v[102:103]
	v_pk_mul_f32 v[100:101], v[8:9], v[104:105]
	v_pk_mul_f32 v[106:107], v[14:15], v[106:107]
	v_pk_mul_f32 v[104:105], v[12:13], v[108:109]
	global_store_dwordx4 v[130:131], v[52:55], off offset:-3072
	global_store_dwordx4 v[130:131], v[96:99], off offset:-2048
	global_store_dwordx4 v[130:131], v[100:103], off offset:-1024
	global_store_dwordx4 v[154:155], v[104:107], off offset:-4096
	v_mbcnt_lo_u32_b32 v52, -1, 0
	v_mbcnt_hi_u32_b32 v52, -1, v52
	v_cvt_f32_fp8_sdwa v136, v208 src0_sel:BYTE_2
	v_cvt_f32_fp8_sdwa v137, v208 src0_sel:BYTE_3
	v_cvt_f32_fp8_e32 v138, v209
	v_cvt_f32_fp8_sdwa v139, v209 src0_sel:BYTE_1
	v_cvt_f32_fp8_sdwa v140, v209 src0_sel:BYTE_2
	v_cvt_f32_fp8_sdwa v141, v209 src0_sel:BYTE_3
	v_lshlrev_b32_e32 v52, 2, v52
	v_cvt_f32_fp8_sdwa v148, v210 src0_sel:BYTE_2
	v_cvt_f32_fp8_sdwa v149, v210 src0_sel:BYTE_3
	s_waitcnt vmcnt(16)
	v_cvt_f32_fp8_e32 v150, v227
	v_cvt_f32_fp8_sdwa v151, v227 src0_sel:BYTE_1
	v_cvt_f32_fp8_sdwa v152, v227 src0_sel:BYTE_2
	v_cvt_f32_fp8_sdwa v153, v227 src0_sel:BYTE_3
	v_pk_fma_f32 v[48:49], v[30:31], v[48:49], v[116:117] op_sel_hi:[0,1,1]
	v_pk_fma_f32 v[116:117], v[30:31], v[146:147], v[122:123] op_sel_hi:[0,1,1]
	v_xor_b32_e32 v122, 64, v52
	s_waitcnt vmcnt(15)
	v_cvt_f32_fp8_e32 v52, v178
	v_cvt_f32_fp8_sdwa v53, v178 src0_sel:BYTE_1
	v_cvt_f32_fp8_sdwa v54, v178 src0_sel:BYTE_2
	v_cvt_f32_fp8_sdwa v55, v178 src0_sel:BYTE_3
	s_waitcnt vmcnt(14)
	v_cvt_f32_fp8_e32 v96, v179
	v_cvt_f32_fp8_sdwa v97, v179 src0_sel:BYTE_1
	v_cvt_f32_fp8_sdwa v98, v179 src0_sel:BYTE_2
	v_cvt_f32_fp8_sdwa v99, v179 src0_sel:BYTE_3
	s_waitcnt vmcnt(13)
	v_cvt_f32_fp8_e32 v100, v180
	v_cvt_f32_fp8_sdwa v101, v180 src0_sel:BYTE_1
	v_cvt_f32_fp8_sdwa v102, v180 src0_sel:BYTE_2
	v_cvt_f32_fp8_sdwa v103, v180 src0_sel:BYTE_3
	s_waitcnt vmcnt(12)
	v_cvt_f32_fp8_e32 v104, v181
	v_cvt_f32_fp8_sdwa v105, v181 src0_sel:BYTE_1
	v_cvt_f32_fp8_sdwa v106, v181 src0_sel:BYTE_2
	v_cvt_f32_fp8_sdwa v107, v181 src0_sel:BYTE_3
	v_pk_fma_f32 v[108:109], v[30:31], v[136:137], v[114:115] op_sel_hi:[0,1,1]
	v_pk_fma_f32 v[110:111], v[30:31], v[138:139], v[120:121] op_sel_hi:[0,1,1]
	v_pk_fma_f32 v[112:113], v[30:31], v[140:141], v[118:119] op_sel_hi:[0,1,1]
	v_pk_fma_f32 v[114:115], v[30:31], v[148:149], v[124:125] op_sel_hi:[0,1,1]
	v_pk_fma_f32 v[118:119], v[30:31], v[152:153], v[128:129] op_sel_hi:[0,1,1]
	v_pk_fma_f32 v[120:121], v[30:31], v[150:151], v[126:127] op_sel_hi:[0,1,1]
	v_pk_fma_f32 v[54:55], v[30:31], v[54:55], v[108:109] op_sel:[1,0,0]
	v_pk_fma_f32 v[48:49], v[30:31], v[52:53], v[48:49] op_sel:[1,0,0]
	v_pk_fma_f32 v[52:53], v[30:31], v[98:99], v[112:113] op_sel:[1,0,0]
	v_pk_fma_f32 v[96:97], v[30:31], v[96:97], v[110:111] op_sel:[1,0,0]
	v_pk_fma_f32 v[98:99], v[30:31], v[100:101], v[116:117] op_sel:[1,0,0]
	v_pk_fma_f32 v[100:101], v[30:31], v[102:103], v[114:115] op_sel:[1,0,0]
	v_pk_fma_f32 v[102:103], v[30:31], v[104:105], v[120:121] op_sel:[1,0,0]
	v_pk_fma_f32 v[104:105], v[30:31], v[106:107], v[118:119] op_sel:[1,0,0]
	v_mov_b64_e32 v[30:31], v[50:51]
	v_pk_fma_f32 v[48:49], v[68:69], v[48:49], v[80:81]
	v_pk_fma_f32 v[50:51], v[70:71], v[54:55], v[82:83]
	v_pk_fma_f32 v[54:55], v[64:65], v[96:97], v[84:85]
	v_pk_fma_f32 v[52:53], v[66:67], v[52:53], v[88:89]
	v_pk_mul_f32 v[64:65], v[50:51], v[50:51]
	v_pk_mul_f32 v[66:67], v[48:49], v[48:49]
	v_pk_mul_f32 v[68:69], v[52:53], v[52:53]
	v_pk_mul_f32 v[70:71], v[54:55], v[54:55]
	v_pk_fma_f32 v[62:63], v[62:63], v[100:101], v[92:93]
	v_pk_fma_f32 v[60:61], v[60:61], v[98:99], v[86:87]
	v_pk_mov_b32 v[82:83], v[66:67], v[64:65] op_sel:[1,0]
	v_mov_b32_e32 v67, v65
	v_pk_mov_b32 v[64:65], v[70:71], v[68:69] op_sel:[1,0]
	v_mov_b32_e32 v71, v69
	v_pk_fma_f32 v[58:59], v[58:59], v[104:105], v[94:95]
	v_pk_fma_f32 v[56:57], v[56:57], v[102:103], v[90:91]
	v_mul_f32_e32 v74, v61, v61
	v_mul_f32_e32 v80, v63, v63
	v_pk_add_f32 v[66:67], v[82:83], v[66:67]
	v_pk_add_f32 v[64:65], v[64:65], v[70:71]
	v_mul_f32_e32 v84, v56, v56
	v_mul_f32_e32 v85, v57, v57
	v_mul_f32_e32 v86, v58, v58
	v_mul_f32_e32 v87, v59, v59
	v_pk_fma_f32 v[68:69], v[60:61], v[60:61], v[74:75] op_sel_hi:[1,1,0]
	v_pk_fma_f32 v[80:81], v[62:63], v[62:63], v[80:81] op_sel_hi:[1,1,0]
	v_pk_add_f32 v[66:67], v[66:67], v[66:67] op_sel:[0,1] op_sel_hi:[1,0]
	v_pk_add_f32 v[64:65], v[64:65], v[64:65] op_sel:[0,1] op_sel_hi:[1,0]
	v_mov_b32_e32 v69, v86
	v_mov_b32_e32 v81, v87
	v_mov_b32_e32 v67, v84
	v_mov_b32_e32 v65, v85
	v_pk_add_f32 v[68:69], v[68:69], v[80:81]
	v_pk_add_f32 v[64:65], v[66:67], v[64:65]
	s_mov_b32 s62, 34
	v_pk_add_f32 v[64:65], v[64:65], v[68:69]
	s_nop 0
	v_add_f32_e32 v64, v64, v65
	s_nop 1
	v_add_f32_dpp v64, v64, v64 quad_perm:[1,0,3,2] row_mask:0xf bank_mask:0xf bound_ctrl:1
	s_nop 1
	v_add_f32_dpp v64, v64, v64 quad_perm:[2,3,0,1] row_mask:0xf bank_mask:0xf bound_ctrl:1
	s_nop 1
	v_add_f32_dpp v64, v64, v64 row_half_mirror row_mask:0xf bank_mask:0xf bound_ctrl:1
	s_nop 1
	v_add_f32_dpp v64, v64, v64 row_mirror row_mask:0xf bank_mask:0xf bound_ctrl:1
	ds_bpermute_b32 v65, v122, v64
	s_waitcnt lgkmcnt(0)
	v_add_f32_e32 v64, v64, v65
	v_mov_b32_e32 v65, v64
	s_nop 1
	v_permlane32_swap_b32 v65, v64
	s_ashr_i32 s63, s62, 31
	v_add_f32_e32 v64, v65, v64
	v_fmamk_f32 v64, v64, 0x3a800000, v73
	v_mul_f32_e32 v65, 0x4b800000, v64
	v_cmp_gt_f32_e64 s[2:3], s74, v64
	s_lshl_b64 s[10:11], s[62:63], 3
	s_add_u32 s10, s0, s10
	v_cndmask_b32_e64 v64, v64, v65, s[2:3]
	v_rsq_f32_e32 v64, v64
	s_addc_u32 s11, s1, s11
	s_load_dwordx2 s[10:11], s[10:11], 0x0
	s_or_b64 s[6:7], vcc, s[6:7]
	v_mul_f32_e32 v65, 0x45800000, v64
	v_cndmask_b32_e64 v64, v64, v65, s[2:3]
	v_pk_mul_f32 v[48:49], v[48:49], v[64:65] op_sel_hi:[1,0]
	v_pk_mul_f32 v[50:51], v[50:51], v[64:65] op_sel_hi:[1,0]
	s_waitcnt lgkmcnt(0)
	v_lshl_add_u64 v[66:67], s[10:11], 0, v[78:79]
	v_lshl_add_u64 v[78:79], v[78:79], 0, s[4:5]
	v_pk_mul_f32 v[68:69], v[54:55], v[64:65] op_sel_hi:[1,0]
	v_pk_mul_f32 v[52:53], v[52:53], v[64:65] op_sel_hi:[1,0]
	v_pk_mul_f32 v[60:61], v[60:61], v[64:65] op_sel_hi:[1,0]
	v_pk_mul_f32 v[62:63], v[62:63], v[64:65] op_sel_hi:[1,0]
	v_pk_mul_f32 v[70:71], v[56:57], v[64:65] op_sel_hi:[1,0]
	v_pk_mul_f32 v[64:65], v[58:59], v[64:65] op_sel_hi:[1,0]
	v_pk_mul_f32 v[50:51], v[2:3], v[50:51]
	v_pk_mul_f32 v[48:49], v[0:1], v[48:49]
	v_pk_mul_f32 v[54:55], v[6:7], v[52:53]
	v_pk_mul_f32 v[52:53], v[4:5], v[68:69]
	v_pk_mul_f32 v[58:59], v[10:11], v[62:63]
	v_pk_mul_f32 v[56:57], v[8:9], v[60:61]
	v_pk_mul_f32 v[62:63], v[14:15], v[64:65]
	v_pk_mul_f32 v[60:61], v[12:13], v[70:71]
	global_store_dwordx4 v[66:67], v[48:51], off offset:-3072
	global_store_dwordx4 v[66:67], v[52:55], off offset:-2048
	global_store_dwordx4 v[66:67], v[56:59], off offset:-1024
	global_store_dwordx4 v[66:67], v[60:63], off
	s_andn2_b64 exec, exec, s[6:7]
	s_cbranch_execnz .LBB0_1977
